# stack: wave index kept in s98 instead of LDS lookup at every fresh_tid, rope positions preloaded before the spatial-weight loop, on top of mods pipeline + rope hoist
# speedup vs baseline: 1.0477x; 1.0045x over previous
_Z4mega5MArgs:
	s_load_dwordx4 s[28:31], s[0:1], 0xe0
	s_load_dword s33, s[0:1], 0xf0
	s_add_u32 s4, s0, 0xf0
	s_addc_u32 s5, s1, 0
	v_lshrrev_b32_e32 v1, 6, v0
	s_nop 1
	v_readfirstlane_b32 s98, v1
	v_and_b32_e32 v1, 63, v0
	v_writelane_b32 v249, s4, 0
	v_cmp_eq_u32_e32 vcc, 0, v1
	s_nop 0
	v_writelane_b32 v249, s5, 1
	s_and_saveexec_b64 s[4:5], vcc
	s_cbranch_execz .LBB0_2
	s_getreg_b32 s3, hwreg(HW_REG_HW_ID, 0, 6)
	s_lshl_b32 s3, s3, 2
	s_and_b32 s3, s3, 0xfc
	s_add_i32 s3, s3, 0
	s_add_i32 s3, s3, 0x25c00
	v_lshrrev_b32_e32 v1, 6, v0
	v_mov_b32_e32 v2, s3
	ds_write_b32 v2, v1

.LBB0_7:
	s_or_b64 exec, exec, s[4:5]
	s_load_dwordx16 s[4:19], s[0:1], 0x80
	s_add_u32 s96, s78, 0x40000
	s_addc_u32 s97, s79, 0
	s_add_u32 s90, s78, 0x8500000
	s_addc_u32 s91, s79, 0
	s_waitcnt lgkmcnt(0)
	v_writelane_b32 v249, s4, 35
	s_cmp_lt_i32 s28, 1
	s_cselect_b64 s[0:1], -1, 0
	v_writelane_b32 v249, s5, 36
	v_writelane_b32 v249, s6, 37
	v_writelane_b32 v249, s7, 38
	v_writelane_b32 v249, s8, 39
	v_writelane_b32 v249, s9, 40
	v_writelane_b32 v249, s10, 41
	v_writelane_b32 v249, s11, 42
	v_writelane_b32 v249, s12, 43
	v_writelane_b32 v249, s13, 44
	v_writelane_b32 v249, s14, 45
	v_writelane_b32 v249, s15, 46
	v_writelane_b32 v249, s16, 47
	v_writelane_b32 v249, s17, 48
	v_writelane_b32 v249, s18, 49
	s_cmp_gt_i32 s29, 0
	v_writelane_b32 v249, s19, 50
	s_cselect_b64 s[4:5], -1, 0
	s_and_b64 s[0:1], s[0:1], s[4:5]
	s_andn2_b64 vcc, exec, s[0:1]
	s_cbranch_vccnz .LBB0_90
	v_mbcnt_lo_u32_b32 v1, -1, 0
	v_mbcnt_hi_u32_b32 v1, -1, v1
	s_cmpk_gt_i32 s2, 0xbf
	s_waitcnt lgkmcnt(0)
	s_mov_b32 s0, s98
	s_nop 1
	v_lshl_add_u32 v28, s0, 6, v1
	s_nop 0
	v_ashrrev_i32_e32 v23, 6, v28
	v_and_b32_e32 v30, 63, v28
	s_cbranch_scc1 .LBB0_18
	v_readlane_b32 s4, v249, 2
	v_readlane_b32 s6, v249, 4
	v_readlane_b32 s7, v249, 5
	v_ashrrev_i32_e32 v29, 31, v28
	v_mov_b32_e32 v0, s6
	v_mov_b32_e32 v1, s7
	v_lshl_add_u64 v[0:1], v[28:29], 2, v[0:1]
	global_load_dword v2, v[0:1], off
	global_load_dword v3, v[0:1], off offset:2048
	s_movk_i32 s0, 0x1000
	v_add_co_u32_e32 v0, vcc, s0, v0
	s_mov_b32 s0, 0xbfb8aa3b
	s_nop 0
	v_addc_co_u32_e32 v1, vcc, 0, v1, vcc
	global_load_dword v4, v[0:1], off
	s_nop 0
	global_load_dword v0, v[0:1], off offset:2048
	s_mov_b32 s3, 0x42ce8ed0
	s_mov_b32 s6, 0xc2b17218
	v_mov_b32_e32 v1, 0x7f800000
	v_readlane_b32 s5, v249, 3
	v_lshl_add_u32 v5, v28, 2, 0
	v_readlane_b32 s8, v249, 6
	v_readlane_b32 s9, v249, 7
	v_readlane_b32 s10, v249, 8
	v_readlane_b32 s11, v249, 9
	v_readlane_b32 s14, v249, 12
	v_mov_b32_e32 v33, 0
	v_lshlrev_b32_e32 v32, 2, v30
	s_mov_b32 s14, s2
	v_readlane_b32 s12, v249, 10
	v_readlane_b32 s13, v249, 11
	v_readlane_b32 s15, v249, 13
	v_readlane_b32 s16, v249, 14
	v_readlane_b32 s17, v249, 15
	v_readlane_b32 s18, v249, 16
	v_readlane_b32 s19, v249, 17
	s_waitcnt vmcnt(3)
	v_mul_f32_e32 v6, 0xbfb8aa3b, v2
	s_waitcnt vmcnt(2)
	v_mul_f32_e32 v7, 0xbfb8aa3b, v3
	v_fma_f32 v8, v2, s0, -v6
	v_rndne_f32_e32 v9, v6
	v_fma_f32 v10, v3, s0, -v7
	v_rndne_f32_e32 v11, v7
	v_fmac_f32_e32 v8, 0xb2a5705f, v2
	v_sub_f32_e32 v6, v6, v9
	v_fmac_f32_e32 v10, 0xb2a5705f, v3
	v_sub_f32_e32 v7, v7, v11
	v_add_f32_e32 v6, v6, v8
	s_waitcnt vmcnt(1)
	v_mul_f32_e32 v12, 0xbfb8aa3b, v4
	v_cvt_i32_f32_e32 v9, v9
	v_add_f32_e32 v7, v7, v10
	v_exp_f32_e32 v6, v6
	v_cvt_i32_f32_e32 v11, v11
	v_fma_f32 v14, v4, s0, -v12
	v_rndne_f32_e32 v15, v12
	v_exp_f32_e32 v7, v7
	v_fmac_f32_e32 v14, 0xb2a5705f, v4
	v_sub_f32_e32 v8, v12, v15
	s_waitcnt vmcnt(0)
	v_mul_f32_e32 v13, 0xbfb8aa3b, v0
	v_add_f32_e32 v8, v8, v14
	v_fma_f32 v16, v0, s0, -v13
	v_rndne_f32_e32 v17, v13
	v_cvt_i32_f32_e32 v10, v15
	v_exp_f32_e32 v8, v8
	v_ldexp_f32 v6, v6, v9
	v_cmp_nlt_f32_e32 vcc, s3, v2
	v_fmac_f32_e32 v16, 0xb2a5705f, v0
	v_sub_f32_e32 v12, v13, v17
	v_ldexp_f32 v7, v7, v11
	v_cndmask_b32_e32 v6, 0, v6, vcc
	v_cmp_nlt_f32_e32 vcc, s3, v3
	v_add_f32_e32 v12, v12, v16
	v_cvt_i32_f32_e32 v13, v17
	v_cndmask_b32_e32 v7, 0, v7, vcc
	v_cmp_ngt_f32_e32 vcc, s6, v2
	v_exp_f32_e32 v12, v12
	v_ldexp_f32 v8, v8, v10
	v_cndmask_b32_e32 v6, v1, v6, vcc
	v_cmp_ngt_f32_e32 vcc, s6, v3
	v_add_f32_e32 v6, 1.0, v6
	v_div_scale_f32 v10, s[0:1], v6, v6, v2
	v_cndmask_b32_e32 v7, v1, v7, vcc
	v_cmp_nlt_f32_e32 vcc, s3, v4
	v_add_f32_e32 v7, 1.0, v7
	v_ldexp_f32 v9, v12, v13
	v_cndmask_b32_e32 v8, 0, v8, vcc
	v_cmp_ngt_f32_e32 vcc, s6, v4
	v_div_scale_f32 v12, s[0:1], v7, v7, v3
	s_nop 0
	v_cndmask_b32_e32 v8, v1, v8, vcc
	v_add_f32_e32 v8, 1.0, v8
	v_rcp_f32_e32 v14, v10
	v_rcp_f32_e32 v15, v12
	v_div_scale_f32 v16, s[4:5], v8, v8, v4
	v_rcp_f32_e32 v18, v16
	v_fma_f32 v19, -v10, v14, 1.0
	v_div_scale_f32 v11, vcc, v2, v6, v2
	v_fma_f32 v20, -v12, v15, 1.0
	v_fmac_f32_e32 v14, v19, v14
	v_div_scale_f32 v13, s[0:1], v3, v7, v3
	v_fmac_f32_e32 v15, v20, v15
	v_fma_f32 v19, -v16, v18, 1.0
	v_mul_f32_e32 v20, v11, v14
	v_mul_f32_e32 v21, v13, v15
	v_fmac_f32_e32 v18, v19, v18
	v_fma_f32 v19, -v10, v20, v11
	v_fma_f32 v22, -v12, v21, v13
	v_fmac_f32_e32 v20, v19, v14
	v_fmac_f32_e32 v21, v22, v15
	v_fma_f32 v10, -v10, v20, v11
	v_fma_f32 v11, -v12, v21, v13
	v_div_fmas_f32 v10, v10, v14, v20
	s_mov_b64 vcc, s[0:1]
	v_div_fixup_f32 v2, v10, v6, v2
	v_div_fmas_f32 v6, v11, v15, v21
	v_div_fixup_f32 v3, v6, v7, v3
	v_cmp_nlt_f32_e32 vcc, s3, v0
	ds_write2st64_b32 v5, v2, v3 offset1:8
	v_div_scale_f32 v17, s[4:5], v4, v8, v4
	v_cndmask_b32_e32 v2, 0, v9, vcc
	v_cmp_ngt_f32_e32 vcc, s6, v0
	v_mul_f32_e32 v24, v17, v18
	v_fma_f32 v19, -v16, v24, v17
	v_cndmask_b32_e32 v1, v1, v2, vcc
	v_add_f32_e32 v1, 1.0, v1
	v_div_scale_f32 v2, s[0:1], v1, v1, v0
	v_rcp_f32_e32 v3, v2
	v_fmac_f32_e32 v24, v19, v18
	v_fma_f32 v12, -v16, v24, v17
	s_mov_b64 vcc, s[4:5]
	v_div_fmas_f32 v6, v12, v18, v24
	v_div_fixup_f32 v4, v6, v8, v4
	v_fma_f32 v6, -v2, v3, 1.0
	v_fmac_f32_e32 v3, v6, v3
	v_div_scale_f32 v6, vcc, v0, v1, v0
	v_mul_f32_e32 v7, v6, v3
	v_fma_f32 v8, -v2, v7, v6
	v_fmac_f32_e32 v7, v8, v3
	v_fma_f32 v2, -v2, v7, v6
	v_div_fmas_f32 v2, v2, v3, v7
	v_div_fixup_f32 v0, v2, v1, v0
	v_lshlrev_b32_e32 v2, 2, v30
	ds_write2st64_b32 v5, v4, v0 offset0:16 offset1:24
	v_add_u32_e32 v0, 0, v2
	v_lshlrev_b32_e32 v3, 9, v23
	v_lshlrev_b32_e32 v1, 7, v23
	v_add_u32_e32 v27, 0, v3
	v_add_u32_e32 v29, v0, v3
	v_and_b32_e32 v3, 0x3fffffc0, v28
	s_movk_i32 s3, 0x6000
	v_lshl_add_u32 v31, v3, 2, v0
	v_mad_i64_i32 v[0:1], s[8:9], v1, s3, 0
	v_or_b32_e32 v0, v0, v2
	s_add_u32 s6, s78, 0x8200
	s_movk_i32 s0, 0x80
	v_lshl_add_u64 v[0:1], s[10:11], 0, v[0:1]
	s_mov_b64 s[8:9], 0xba000
	s_addc_u32 s7, s79, 0
	v_cmp_gt_i32_e64 s[0:1], s0, v28
	v_cmp_eq_u32_e64 s[4:5], 0, v28
	v_lshl_add_u64 v[34:35], v[0:1], 0, s[8:9]
	s_mov_b64 s[8:9], 0xc0000
	s_waitcnt lgkmcnt(0)
	s_barrier
	s_branch .LBB0_11

.LBB0_39:
	s_or_b64 exec, exec, s[6:7]
	v_lshl_add_u32 v0, s2, 9, v28
	s_mov_b32 s0, 0x20000
	s_lshl_b32 s6, s33, 9
	v_readlane_b32 s48, v249, 6
	v_readlane_b32 s49, v249, 7
	v_mov_b32_e32 v44, v0
	v_min_i32_e32 v45, 0x7ffff, v44
	v_lshrrev_b32_e32 v45, 5, v45
	v_lshlrev_b32_e32 v45, 2, v45
	s_nop 1
	global_load_dword v40, v45, s[48:49]
	v_add_u32_e32 v44, s6, v44
	v_min_i32_e32 v45, 0x7ffff, v44
	v_lshrrev_b32_e32 v45, 5, v45
	v_lshlrev_b32_e32 v45, 2, v45
	global_load_dword v41, v45, s[48:49]
	v_add_u32_e32 v44, s6, v44
	v_min_i32_e32 v45, 0x7ffff, v44
	v_lshrrev_b32_e32 v45, 5, v45
	v_lshlrev_b32_e32 v45, 2, v45
	global_load_dword v42, v45, s[48:49]
	v_add_u32_e32 v44, s6, v44
	v_min_i32_e32 v45, 0x7ffff, v44
	v_lshrrev_b32_e32 v45, 5, v45
	v_lshlrev_b32_e32 v45, 2, v45
	global_load_dword v43, v45, s[48:49]
	s_mov_b32 s99, 0
	v_cmp_gt_i32_e32 vcc, s0, v0
	s_and_saveexec_b64 s[0:1], vcc
	s_cbranch_execz .LBB0_44
	v_readlane_b32 s8, v249, 35
	v_readlane_b32 s9, v249, 36
	v_readlane_b32 s10, v249, 37
	v_readlane_b32 s11, v249, 38
	v_ashrrev_i32_e32 v1, 31, v0
	v_readlane_b32 s12, v249, 39
	v_readlane_b32 s13, v249, 40
	v_mov_b32_e32 v2, s8
	v_mov_b32_e32 v3, s9
	s_ashr_i32 s7, s6, 31
	v_lshl_add_u64 v[4:5], v[0:1], 1, s[78:79]
	s_mov_b64 s[10:11], 0x500000
	v_and_b32_e32 v6, 0x7f, v28
	v_lshl_add_u64 v[2:3], v[0:1], 2, v[2:3]
	s_lshl_b64 s[8:9], s[6:7], 2
	v_lshl_add_u64 v[4:5], v[4:5], 0, s[10:11]
	s_lshl_b64 s[10:11], s[6:7], 1
	s_mov_b64 s[12:13], 0
	s_movk_i32 s5, 0x7fff
	s_mov_b32 s7, 0x1ffff
	v_mov_b32_e32 v1, v0
	v_readlane_b32 s14, v249, 41
	v_readlane_b32 s15, v249, 42
	v_readlane_b32 s16, v249, 43
	v_readlane_b32 s17, v249, 44
	v_readlane_b32 s18, v249, 45
	v_readlane_b32 s19, v249, 46
	v_readlane_b32 s20, v249, 47
	v_readlane_b32 s21, v249, 48
	v_readlane_b32 s22, v249, 49
	v_readlane_b32 s23, v249, 50
	s_branch .LBB0_42

.Lrope_f_done:
	s_or_b64 exec, exec, s[20:21]
	s_waitcnt vmcnt(0)
	s_branch .LBB0_58
.LBB0_58:
	v_ashrrev_i32_e32 v6, 5, v0
	v_readlane_b32 s48, v249, 2
	v_ashrrev_i32_e32 v7, 31, v6
	v_readlane_b32 s52, v249, 6
	v_readlane_b32 s53, v249, 7
	v_ashrrev_i32_e32 v1, 31, v0
	v_readlane_b32 s49, v249, 3
	v_lshl_add_u64 v[6:7], v[6:7], 2, s[52:53]
	s_cmp_lt_u32 s99, 4
	s_cbranch_scc1 .Lrope_pre
	global_load_dword v5, v[6:7], off
	s_waitcnt vmcnt(0)
	s_branch .Lrope_have
.Lrope_pre:
	v_mov_b32_e32 v5, v40
	v_mov_b32_e32 v40, v41
	v_mov_b32_e32 v41, v42
	v_mov_b32_e32 v42, v43
.Lrope_have:
	s_add_i32 s99, s99, 1
	v_lshlrev_b64 v[6:7], 2, v[0:1]
	v_add_u32_e32 v0, s6, v0
	v_cmp_lt_i32_e64 s[0:1], s5, v0
	v_lshl_add_u64 v[8:9], s[10:11], 0, v[6:7]
	s_or_b64 s[14:15], s[0:1], s[14:15]
	v_readlane_b32 s50, v249, 4
	v_readlane_b32 s51, v249, 5
	v_readlane_b32 s54, v249, 8
	v_readlane_b32 s55, v249, 9
	v_readlane_b32 s56, v249, 10
	v_readlane_b32 s57, v249, 11
	v_readlane_b32 s58, v249, 12
	v_readlane_b32 s59, v249, 13
	v_readlane_b32 s60, v249, 14
	v_readlane_b32 s61, v249, 15
	v_readlane_b32 s62, v249, 16
	v_readlane_b32 s63, v249, 17
	v_lshl_add_u64 v[6:7], s[12:13], 0, v[6:7]
	v_cvt_f64_i32_e32 v[10:11], v5
	v_mul_f64 v[2:3], v[14:15], v[10:11]
	v_mul_f64 v[10:11], v[2:3], s[18:19]
	v_floor_f64_e32 v[10:11], v[10:11]
	v_fma_f64 v[2:3], v[2:3], s[18:19], -v[10:11]
	v_cvt_f32_f64_e32 v1, v[2:3]
	v_cos_f32_e32 v2, v1
	v_sin_f32_e32 v1, v1
	global_store_dword v[8:9], v2, off
	global_store_dword v[6:7], v1, off
	s_andn2_b64 exec, exec, s[14:15]
	s_cbranch_execz .LBB0_63

.LBB0_63:
	s_or_b64 exec, exec, s[8:9]
	s_barrier
	s_waitcnt lgkmcnt(0)
	s_mov_b32 s0, s98
	v_mbcnt_lo_u32_b32 v0, -1, 0
	v_mbcnt_hi_u32_b32 v0, -1, v0
	s_nop 1
	v_lshl_add_u32 v0, s0, 6, v0
	s_nop 0
	v_cmp_eq_u32_e32 vcc, 0, v0
	s_and_saveexec_b64 s[0:1], vcc
	s_cbranch_execz .LBB0_72
	s_add_u32 s6, s78, 0x8200
	s_addc_u32 s7, s79, 0
	s_mov_b32 s5, 0x400001
	v_mov_b32_e32 v0, 0
	s_movk_i32 s10, 0xbf
	s_movk_i32 s11, 0xc0
	s_branch .LBB0_66

.LBB0_72:
	s_or_b64 exec, exec, s[0:1]
	s_waitcnt lgkmcnt(0)
	s_mov_b32 s0, s98
	v_mbcnt_lo_u32_b32 v0, -1, 0
	v_mbcnt_hi_u32_b32 v0, -1, v0
	s_nop 1
	v_lshl_add_u32 v0, s0, 6, v0
	s_nop 0
	v_cmp_eq_u32_e32 vcc, 0, v0
	s_and_saveexec_b64 s[0:1], vcc
	s_cbranch_execz .LBB0_74
	s_waitcnt vmcnt(0)
	buffer_inv sc1
	s_waitcnt vmcnt(0)
.LBB0_74:
	s_or_b64 exec, exec, s[0:1]
	s_barrier
	v_mbcnt_lo_u32_b32 v1, -1, 0
	v_mbcnt_hi_u32_b32 v1, -1, v1
	s_movk_i32 s20, 0x4000
	s_waitcnt lgkmcnt(0)
	s_mov_b32 s0, s98
	s_nop 1
	v_lshl_add_u32 v1, s0, 6, v1
	s_nop 0
	v_ashrrev_i32_e32 v0, 6, v1
	v_add_u32_e32 v92, s4, v0
	v_cmp_gt_i32_e32 vcc, s20, v92
	s_and_saveexec_b64 s[6:7], vcc
	s_cbranch_execz .LBB0_89
	v_lshlrev_b32_e32 v2, 2, v1
	v_and_b32_e32 v1, 63, v1
	v_lshlrev_b32_e32 v70, 3, v1
	v_ashrrev_i32_e32 v1, 31, v0
	s_ashr_i32 s5, s4, 31
	v_and_b32_e32 v2, 0xfc, v2
	v_readlane_b32 s48, v249, 2
	v_add_u32_e32 v10, s3, v92
	v_lshl_add_u64 v[0:1], v[0:1], 0, s[4:5]
	v_mov_b32_e32 v65, 0
	v_lshlrev_b32_e32 v64, 2, v2
	v_readlane_b32 s49, v249, 3
	s_lshl_b32 s8, s33, 5
	v_ashrrev_i32_e32 v11, 31, v10
	v_lshlrev_b64 v[74:75], 12, v[0:1]
	v_lshlrev_b64 v[0:1], 11, v[0:1]
	v_lshl_add_u64 v[66:67], s[48:49], 0, v[64:65]
	v_or_b32_e32 v4, 0x100, v2
	v_or_b32_e32 v6, 0x200, v2
	v_or_b32_e32 v8, 0x300, v2
	v_lshlrev_b32_e32 v64, 1, v2
	v_lshlrev_b64 v[12:13], 11, v[10:11]
	s_ashr_i32 s9, s8, 31
	v_lshl_add_u64 v[0:1], s[78:79], 0, v[0:1]
	s_mov_b64 s[0:1], 0x8500400
	v_lshl_add_u64 v[68:69], s[90:91], 0, v[64:65]
	s_lshl_b32 s21, s33, 4
	s_mul_i32 s22, s33, 24
	v_mov_b32_e32 v71, v65
	v_lshl_add_u64 v[72:73], s[78:79], 0, v[12:13]
	s_lshl_b64 s[10:11], s[8:9], 11
	s_lshl_b64 s[12:13], s[8:9], 12
	v_lshlrev_b64 v[76:77], 12, v[10:11]
	v_lshl_add_u64 v[78:79], v[0:1], 0, s[0:1]
	s_mov_b64 s[14:15], 0
	s_mov_b64 s[16:17], 0x1000
	v_lshlrev_b32_e32 v64, 2, v2
	v_lshlrev_b32_e32 v80, 2, v4
	v_lshlrev_b32_e32 v82, 2, v6
	v_lshlrev_b32_e32 v84, 2, v8
	s_mov_b32 s9, 0x8500000
	s_movk_i32 s23, 0x3fff
	v_mov_b64_e32 v[86:87], v[66:67]
	v_readlane_b32 s50, v249, 4
	v_readlane_b32 s51, v249, 5
	v_readlane_b32 s52, v249, 6
	v_readlane_b32 s53, v249, 7
	v_readlane_b32 s54, v249, 8
	v_readlane_b32 s55, v249, 9
	v_readlane_b32 s56, v249, 10
	v_readlane_b32 s57, v249, 11
	v_readlane_b32 s58, v249, 12
	v_readlane_b32 s59, v249, 13
	v_readlane_b32 s60, v249, 14
	v_readlane_b32 s61, v249, 15
	v_readlane_b32 s62, v249, 16
	v_readlane_b32 s63, v249, 17
	s_branch .LBB0_77

.LBB0_90:
	s_cmp_lt_i32 s28, 2
	s_cselect_b64 s[0:1], -1, 0
	s_cmp_gt_i32 s29, 2
	s_cselect_b64 s[4:5], -1, 0
	s_and_b64 s[0:1], s[0:1], s[4:5]
	s_andn2_b64 vcc, exec, s[0:1]
	s_cbranch_vccnz .LBB0_240
	s_waitcnt vmcnt(0)
	s_barrier
	s_waitcnt lgkmcnt(0)
	s_mov_b32 s0, s98
	v_mbcnt_lo_u32_b32 v0, -1, 0
	v_mbcnt_hi_u32_b32 v0, -1, v0
	s_nop 1
	v_lshl_add_u32 v0, s0, 6, v0
	s_nop 0
	v_cmp_eq_u32_e32 vcc, 0, v0
	s_and_saveexec_b64 s[6:7], vcc
	s_cbranch_execz .LBB0_119
	s_add_i32 s0, 0, 0x24800
	v_mov_b32_e32 v0, s0
	s_waitcnt vmcnt(0) expcnt(0) lgkmcnt(0)
	ds_read_b32 v1, v0
	s_add_i32 s0, 0, 0x24804
	v_mov_b32_e32 v0, s0
	ds_read_b32 v0, v0
	s_waitcnt lgkmcnt(1)
	v_cmp_ne_u32_e32 vcc, 0, v1
	s_cbranch_vccz .Lcensus_0

.LBB0_119:
	s_or_b64 exec, exec, s[6:7]
	s_waitcnt lgkmcnt(0)
	s_mov_b32 s0, s98
	v_mbcnt_lo_u32_b32 v0, -1, 0
	v_mbcnt_hi_u32_b32 v0, -1, v0
	s_nop 1
	v_lshl_add_u32 v6, s0, 6, v0
	s_nop 0
	v_ashrrev_i32_e32 v0, 6, v6
	v_add_u32_e32 v0, -1, v0
	v_cmp_gt_u32_e32 vcc, 3, v0
	s_and_saveexec_b64 s[6:7], vcc
	s_cbranch_execz .LBB0_209
	v_mad_u64_u32 v[2:3], s[0:1], s2, 3, v[0:1]
	s_movk_i32 s0, 0x1d00
	s_nop 0
	v_cmp_gt_i32_e32 vcc, s0, v2
	s_and_b64 exec, exec, vcc
	s_cbranch_execz .LBB0_209
	s_movk_i32 s1, 0x1100
	s_movk_i32 s0, 0xbff
	v_mov_b32_e32 v1, 0xffffef00
	v_mov_b32_e32 v3, 0xfffff400
	v_cmp_gt_u32_e32 vcc, s1, v2
	v_mov_b32_e32 v4, 0x280
	s_nop 0
	v_cndmask_b32_e32 v1, v1, v3, vcc
	v_cndmask_b32_e64 v3, 2, 1, vcc
	v_cmp_lt_i32_e32 vcc, s0, v2
	s_nop 1
	v_cndmask_b32_e32 v1, v4, v1, vcc
	v_cndmask_b32_e32 v3, 0, v3, vcc
	v_add_u32_e32 v1, v1, v2
	v_cmp_lt_i32_e32 vcc, 0, v3
	s_and_saveexec_b64 s[0:1], vcc
	s_xor_b64 s[0:1], exec, s[0:1]
	s_cbranch_execz .LBB0_127
	v_cmp_ne_u32_e32 vcc, 1, v3
	s_and_saveexec_b64 s[8:9], vcc
	s_xor_b64 s[8:9], exec, s[8:9]
	s_movk_i32 s3, 0x800
	v_mov_b32_e32 v2, 0x1380
	v_mov_b32_e32 v3, 0xf80
	v_cmp_gt_i32_e32 vcc, s3, v1
	s_nop 1
	v_cndmask_b32_e32 v2, v2, v3, vcc
	v_add_u32_e32 v1, v2, v1
	s_andn2_saveexec_b64 s[8:9], s[8:9]
	v_add_u32_e32 v1, 0x280, v1
	s_or_b64 exec, exec, s[8:9]

.LBB0_209:
	s_or_b64 exec, exec, s[6:7]
	s_waitcnt lgkmcnt(0)
	s_mov_b32 s0, s98
	v_mbcnt_lo_u32_b32 v0, -1, 0
	v_mbcnt_hi_u32_b32 v0, -1, v0
	s_nop 1
	v_lshl_add_u32 v0, s0, 6, v0
	s_nop 0
	v_cmp_eq_u32_e32 vcc, 0, v0
	s_and_saveexec_b64 s[0:1], vcc
	s_cbranch_execz .LBB0_239
	s_add_i32 s3, 0, 0x24808
	v_mov_b32_e32 v0, s3
	s_add_i32 s3, 0, 0x2480c
	v_mov_b32_e32 v1, s3
	ds_read_b32 v0, v0
	ds_read_b32 v1, v1
	s_waitcnt lgkmcnt(0)
	v_cmp_eq_u32_e32 vcc, 0, v1
	s_cbranch_vccnz .LBB0_220
	v_mov_b32_e32 v1, 0x3000
	s_add_i32 s3, 0, 0x24804
	v_mov_b32_e32 v3, s3
	ds_read_b32 v3, v3
	global_load_dword v1, v1, s[94:95] offset:1024 sc1
	s_waitcnt lgkmcnt(0)
	v_mul_lo_u32 v0, v0, v3
	s_add_u32 s6, s94, 0x3400
	s_addc_u32 s7, s95, 0
	s_waitcnt vmcnt(0)
	v_cmp_ge_u32_e32 vcc, v1, v0
	s_cbranch_vccnz .LBB0_225
	s_mov_b32 s3, 1
	v_mov_b32_e32 v1, 0
	s_branch .LBB0_214

.LBB0_240:
	s_cmp_lt_i32 s28, 3
	s_cselect_b64 s[6:7], -1, 0
	s_and_b64 s[0:1], s[6:7], s[4:5]
	s_andn2_b64 vcc, exec, s[0:1]
	s_mov_b64 s[0:1], s[28:29]
	v_writelane_b32 v249, s0, 51
	s_nop 1
	v_writelane_b32 v249, s1, 52
	v_writelane_b32 v249, s2, 53
	v_writelane_b32 v249, s3, 54
	v_writelane_b32 v249, s72, 55
	s_nop 1
	v_writelane_b32 v249, s73, 56
	v_writelane_b32 v249, s74, 57
	v_writelane_b32 v249, s75, 58
	v_writelane_b32 v249, s76, 59
	v_writelane_b32 v249, s77, 60
	v_writelane_b32 v249, s78, 61
	v_writelane_b32 v249, s79, 62
	v_writelane_b32 v249, s90, 63
	s_nop 1
	v_writelane_b32 v248, s91, 0
	s_cbranch_vccnz .LBB0_381
	s_cmpk_lt_i32 s2, 0x180
	s_cselect_b64 s[0:1], -1, 0
	s_cmpk_gt_i32 s2, 0x17f
	s_waitcnt lgkmcnt(0)
	s_mov_b32 s3, s98
	v_mbcnt_lo_u32_b32 v0, -1, 0
	v_mbcnt_hi_u32_b32 v0, -1, v0
	s_nop 1
	v_lshl_add_u32 v0, s3, 6, v0
	s_nop 0
	v_readfirstlane_b32 s18, v0
	s_cbranch_scc1 .LBB0_243
	s_ashr_i32 s3, s2, 31
	s_lshr_b32 s3, s3, 29
	s_add_i32 s3, s2, s3
	s_ashr_i32 s4, s3, 3
	s_and_b32 s3, s3, -8
	s_sub_i32 s3, s2, s3
	s_cmp_lt_i32 s3, 0
	s_cselect_b32 s5, 49, 48
	s_mul_i32 s3, s3, s5
	s_add_i32 s3, s3, s4
	s_mul_hi_i32 s4, s3, 0x2aaaaaab
	s_lshr_b32 s5, s4, 31
	s_ashr_i32 s4, s4, 3
	s_add_i32 s4, s4, s5
	s_lshl_b32 s5, s4, 3
	s_mul_i32 s4, s4, 48
	s_sub_i32 s3, s3, s4
	s_bfe_i32 s4, s3, 0x80000
	s_bfe_u32 s4, s4, 0x3000c
	s_add_i32 s4, s3, s4
	s_bfe_i32 s8, s4, 0x80000
	s_and_b32 s4, s4, 0xf8
	s_sub_i32 s3, s3, s4
	s_sext_i32_i16 s8, s8
	s_sext_i32_i8 s3, s3
	s_add_i32 s4, s5, s3
	s_ashr_i32 s36, s8, 3

.LBB0_328:
	s_andn2_b64 vcc, exec, s[12:13]
	s_cbranch_vccnz .LBB0_380
	s_ashr_i32 s0, s2, 1
	s_add_i32 s0, s33, s0
	s_cmpk_gt_i32 s0, 0x17f
	s_waitcnt lgkmcnt(0)
	s_mov_b32 s1, s98
	v_mbcnt_lo_u32_b32 v0, -1, 0
	v_mbcnt_hi_u32_b32 v0, -1, v0
	s_nop 1
	v_lshl_add_u32 v0, s1, 6, v0
	s_nop 0
	v_readfirstlane_b32 s1, v0
	s_cbranch_scc1 .LBB0_380
	v_bfe_i32 v3, v0, 27, 1
	v_lshlrev_b32_e32 v1, 4, v0
	v_lshrrev_b32_e32 v3, 22, v3
	v_add_u32_e32 v3, v1, v3
	v_and_b32_e32 v3, 0xfffffc00, v3
	v_ashrrev_i32_e32 v2, 31, v0
	v_sub_u32_e32 v1, v1, v3
	v_lshrrev_b32_e32 v2, 26, v2
	v_lshrrev_b32_e32 v3, 4, v1
	v_add_u32_e32 v2, v0, v2
	v_bitop3_b32 v3, v3, v1, 32 bitop3:0x6c
	v_ashrrev_i32_e32 v1, 31, v1
	v_ashrrev_i32_e32 v2, 6, v2
	v_lshrrev_b32_e32 v1, 26, v1
	v_lshlrev_b32_e32 v4, 3, v2
	v_add_u32_e32 v1, v3, v1
	v_and_b32_e32 v4, -16, v4
	v_ashrrev_i32_e32 v1, 6, v1
	v_add_u32_e32 v4, v1, v4
	v_mul_i32_i24_e32 v5, 64, v1
	v_and_b32_e32 v1, 3, v1
	s_mov_b32 s4, 0x1fffe0
	v_and_or_b32 v1, v4, s4, v1
	s_ashr_i32 s4, s0, 31
	s_lshr_b32 s4, s4, 29
	s_add_i32 s4, s0, s4
	s_ashr_i32 s16, s1, 6
	s_ashr_i32 s5, s4, 3
	s_and_b32 s4, s4, -8
	s_and_b32 s20, s2, 1
	s_ashr_i32 s15, s1, 8
	s_lshl_b32 s14, s16, 10
	s_sub_i32 s0, s0, s4
	s_lshl_b32 s4, s20, 7
	s_cmp_lt_i32 s0, 0
	s_cselect_b32 s12, 49, 48
	s_mul_i32 s0, s0, s12
	s_add_i32 s0, s0, s5
	s_mul_hi_i32 s5, s0, 0x2aaaaaab
	s_lshr_b32 s12, s5, 31
	s_ashr_i32 s5, s5, 3
	s_add_i32 s5, s5, s12
	s_lshl_b32 s12, s5, 3
	s_mul_i32 s5, s5, 48
	s_sub_i32 s5, s0, s5
	s_bfe_i32 s0, s5, 0x80000
	s_bfe_u32 s0, s0, 0x3000c
	s_add_i32 s13, s5, s0
	s_bfe_i32 s0, s13, 0x80000
	s_and_b32 s13, s13, 0xf8
	s_sub_i32 s5, s5, s13
	s_sext_i32_i8 s5, s5
	s_add_i32 s21, s12, s5
	s_lshl_b32 s5, s21, 8
	s_or_b32 s4, s5, s4
	s_sext_i32_i16 s0, s0
	s_ashr_i32 s5, s4, 31
	s_lshr_b32 s0, s0, 3
	s_lshl_b64 s[4:5], s[4:5], 11
	v_sub_u32_e32 v3, v3, v5
	v_mov_b32_e32 v5, 1
	s_add_u32 s4, s90, s4
	v_lshlrev_b32_e32 v2, 5, v2
	v_ashrrev_i16_sdwa v3, v5, sext(v3) dst_sel:DWORD dst_unused:UNUSED_PAD src0_sel:DWORD src1_sel:BYTE_0
	v_lshlrev_b32_e32 v5, 1, v4
	v_lshrrev_b32_e32 v6, 2, v4
	s_addc_u32 s5, s91, s5
	s_bfe_i64 s[12:13], s[0:1], 0x100000
	v_and_b32_e32 v2, 32, v2
	v_bfe_i32 v3, v3, 0, 16
	v_and_b32_e32 v5, 24, v5
	v_and_b32_e32 v6, 4, v6
	s_lshl_b64 s[12:13], s[12:13], 19
	v_or3_b32 v1, v1, v6, v5
	v_add_lshl_u32 v2, v2, v3, 1
	s_add_u32 s12, s49, s12
	v_lshl_add_u32 v36, v1, 11, v2
	s_addc_u32 s13, s50, s13
	s_add_i32 s23, s14, 0
	s_mov_b64 s[18:19], s[12:13]
	s_add_i32 m0, s23, 0x10000
	v_lshl_add_u32 v37, v4, 11, v2
	global_load_lds_dwordx4 v36, s[18:19]
	s_add_u32 s18, s12, 0x20000
	s_addc_u32 s19, s13, 0
	s_add_i32 m0, s23, 0x12000
	s_nop 0
	global_load_lds_dwordx4 v36, s[18:19]
	s_add_i32 m0, s23, 0x14000
	s_add_u32 s18, s12, 0x40000
	s_addc_u32 s19, s13, 0
	s_nop 0
	global_load_lds_dwordx4 v36, s[18:19]
	s_add_u32 s18, s12, 0x60000
	s_addc_u32 s19, s13, 0
	s_add_i32 m0, s23, 0x16000
	s_nop 0
	global_load_lds_dwordx4 v36, s[18:19]
	s_mov_b64 s[18:19], s[4:5]
	s_mov_b32 m0, s23
	s_nop 0
	global_load_lds_dwordx4 v37, s[18:19]
	s_add_u32 s18, s4, 0x20000
	s_addc_u32 s19, s5, 0
	s_add_i32 s24, s23, 0x2000
	s_mov_b32 m0, s24
	s_cmp_lg_u32 s15, 1
	global_load_lds_dwordx4 v37, s[18:19]
	s_cbranch_scc1 .LBB0_332
	s_barrier

.LBB0_381:
	s_cmp_gt_i32 s29, 3
	s_cselect_b64 s[4:5], -1, 0
	s_and_b64 s[0:1], s[6:7], s[4:5]
	s_andn2_b64 vcc, exec, s[0:1]
	s_cbranch_vccnz .LBB0_531
	s_waitcnt vmcnt(0)
	s_waitcnt lgkmcnt(0)
	s_barrier
	s_waitcnt lgkmcnt(0)
	s_mov_b32 s0, s98
	v_mbcnt_lo_u32_b32 v0, -1, 0
	v_mbcnt_hi_u32_b32 v0, -1, v0
	s_nop 1
	v_lshl_add_u32 v0, s0, 6, v0
	s_nop 0
	v_cmp_eq_u32_e32 vcc, 0, v0
	s_and_saveexec_b64 s[6:7], vcc
	s_cbranch_execz .LBB0_410
	s_add_i32 s0, 0, 0x24800
	v_mov_b32_e32 v0, s0
	s_waitcnt vmcnt(0) expcnt(0) lgkmcnt(0)
	ds_read_b32 v1, v0
	s_add_i32 s0, 0, 0x24804
	v_mov_b32_e32 v0, s0
	ds_read_b32 v0, v0
	s_waitcnt lgkmcnt(1)
	v_cmp_ne_u32_e32 vcc, 0, v1
	s_cbranch_vccz .Lcensus_1

.LBB0_410:
	s_or_b64 exec, exec, s[6:7]
	s_waitcnt lgkmcnt(0)
	s_mov_b32 s0, s98
	v_mbcnt_lo_u32_b32 v0, -1, 0
	v_mbcnt_hi_u32_b32 v0, -1, v0
	s_nop 1
	v_lshl_add_u32 v6, s0, 6, v0
	s_nop 0
	v_ashrrev_i32_e32 v0, 6, v6
	v_add_u32_e32 v0, -1, v0
	v_cmp_gt_u32_e32 vcc, 3, v0
	s_and_saveexec_b64 s[6:7], vcc
	s_cbranch_execz .LBB0_500
	s_add_i32 s0, s33, s2
	v_mad_u64_u32 v[2:3], s[0:1], s0, 3, v[0:1]
	s_movk_i32 s0, 0x1d00
	s_nop 0
	v_cmp_gt_i32_e32 vcc, s0, v2
	s_and_b64 exec, exec, vcc
	s_cbranch_execz .LBB0_500
	s_movk_i32 s1, 0x1100
	s_movk_i32 s0, 0xbff
	v_mov_b32_e32 v1, 0xffffef00
	v_mov_b32_e32 v3, 0xfffff400
	v_cmp_gt_u32_e32 vcc, s1, v2
	v_mov_b32_e32 v4, 0x280
	s_nop 0
	v_cndmask_b32_e32 v1, v1, v3, vcc
	v_cndmask_b32_e64 v3, 2, 1, vcc
	v_cmp_lt_i32_e32 vcc, s0, v2
	s_nop 1
	v_cndmask_b32_e32 v1, v4, v1, vcc
	v_cndmask_b32_e32 v3, 0, v3, vcc
	v_add_u32_e32 v1, v1, v2
	v_cmp_lt_i32_e32 vcc, 0, v3
	s_and_saveexec_b64 s[0:1], vcc
	s_xor_b64 s[0:1], exec, s[0:1]
	s_cbranch_execz .LBB0_418
	v_cmp_ne_u32_e32 vcc, 1, v3
	s_and_saveexec_b64 s[8:9], vcc
	s_xor_b64 s[8:9], exec, s[8:9]
	s_movk_i32 s3, 0x800
	v_mov_b32_e32 v2, 0x1380
	v_mov_b32_e32 v3, 0xf80
	v_cmp_gt_i32_e32 vcc, s3, v1
	s_nop 1
	v_cndmask_b32_e32 v2, v2, v3, vcc
	v_add_u32_e32 v1, v2, v1
	s_andn2_saveexec_b64 s[8:9], s[8:9]
	v_add_u32_e32 v1, 0x280, v1
	s_or_b64 exec, exec, s[8:9]

.LBB0_531:
	s_cmp_lt_i32 s28, 4
	s_cselect_b64 s[84:85], -1, 0
	s_and_b64 s[0:1], s[84:85], s[4:5]
	s_andn2_b64 vcc, exec, s[0:1]
	s_cbranch_vccnz .LBB0_561
	s_cmpk_gt_i32 s2, 0x1ff
	s_waitcnt lgkmcnt(0)
	s_mov_b32 s0, s98
	v_mbcnt_lo_u32_b32 v0, -1, 0
	v_mbcnt_hi_u32_b32 v0, -1, v0
	s_nop 1
	v_lshl_add_u32 v2, s0, 6, v0
	s_nop 0
	v_readfirstlane_b32 s16, v2
	s_cbranch_scc1 .LBB0_560
	v_readlane_b32 s4, v249, 55
	v_readlane_b32 s10, v249, 61
	v_readlane_b32 s11, v249, 62
	s_add_u32 s86, s10, 0x14500000
	s_addc_u32 s87, s11, 0
	s_add_u32 s88, s10, 0x14d00000
	s_addc_u32 s89, s11, 0
	s_ashr_i32 s0, s2, 8
	s_bfe_u32 s3, s2, 0x60002
	s_ashr_i32 s1, s0, 31
	s_lshl_b64 s[10:11], s[0:1], 13
	s_lshl_b32 s0, s3, 7
	s_or_b32 s10, s10, s0
	s_cmp_lg_u32 s3, 0
	s_cselect_b64 s[14:15], -1, 0
	s_lshl_b32 s0, s2, 7
	s_and_b32 s0, s0, 0x180
	s_add_u32 s12, s86, s0
	v_mov_b32_e32 v80, 0
	v_readlane_b32 s8, v249, 59
	s_addc_u32 s13, s87, 0
	v_ashrrev_i32_e32 v112, 3, v2
	s_movk_i32 s3, 0x7f
	v_mov_b32_e32 v82, v80
	v_mov_b32_e32 v83, v80
	v_readlane_b32 s6, v249, 57
	v_readlane_b32 s7, v249, 58
	v_readlane_b32 s9, v249, 60
	s_add_u32 s8, s88, s0
	v_cmp_lt_i32_e64 s[0:1], s3, v112
	v_mov_b32_e32 v81, v80
	v_mov_b64_e32 v[86:87], v[82:83]
	v_mov_b64_e32 v[90:91], v[82:83]
	v_readlane_b32 s5, v249, 56
	s_addc_u32 s9, s89, 0
	s_or_b64 s[6:7], s[14:15], s[0:1]
	v_ashrrev_i32_e32 v113, 31, v112
	v_lshlrev_b32_e32 v3, 4, v2
	v_mov_b64_e32 v[84:85], v[80:81]
	v_mov_b64_e32 v[88:89], v[80:81]
	s_and_saveexec_b64 s[4:5], s[6:7]
	s_cbranch_execz .LBB0_535
	v_lshl_add_u64 v[0:1], s[10:11], 0, v[112:113]
	s_mov_b32 s6, 0xffff0000
	v_lshlrev_b64 v[0:1], 9, v[0:1]
	s_mov_b32 s7, -1
	v_lshl_add_u64 v[0:1], v[0:1], 0, s[6:7]
	v_lshl_add_u64 v[4:5], s[12:13], 0, v[0:1]
	v_and_b32_e32 v6, 0x70, v3
	v_mov_b32_e32 v7, v80
	v_lshl_add_u64 v[4:5], v[4:5], 0, v[6:7]
	v_lshl_add_u64 v[0:1], s[8:9], 0, v[0:1]
	v_lshl_add_u64 v[0:1], v[0:1], 0, v[6:7]
	global_load_dwordx4 v[88:91], v[4:5], off
	global_load_dwordx4 v[84:87], v[0:1], off

.LBB0_561:
	v_readlane_b32 s4, v249, 51
	v_readlane_b32 s5, v249, 52
	v_readlane_b32 s6, v249, 53
	v_readlane_b32 s7, v249, 54
	s_cmp_gt_i32 s5, 4
	s_cselect_b64 s[6:7], -1, 0
	s_and_b64 s[0:1], s[84:85], s[6:7]
	s_andn2_b64 vcc, exec, s[0:1]
	s_cbranch_vccnz .LBB0_711
	s_waitcnt vmcnt(0)
	s_waitcnt lgkmcnt(0)
	s_barrier
	s_waitcnt lgkmcnt(0)
	s_mov_b32 s0, s98
	v_mbcnt_lo_u32_b32 v0, -1, 0
	v_mbcnt_hi_u32_b32 v0, -1, v0
	s_nop 1
	v_lshl_add_u32 v0, s0, 6, v0
	s_nop 0
	v_cmp_eq_u32_e32 vcc, 0, v0
	s_and_saveexec_b64 s[4:5], vcc
	s_cbranch_execz .LBB0_590
	s_add_i32 s0, 0, 0x24800
	v_mov_b32_e32 v0, s0
	s_waitcnt vmcnt(0) expcnt(0) lgkmcnt(0)
	ds_read_b32 v1, v0
	s_add_i32 s0, 0, 0x24804
	v_mov_b32_e32 v0, s0
	ds_read_b32 v0, v0
	s_waitcnt lgkmcnt(1)
	v_cmp_ne_u32_e32 vcc, 0, v1
	s_cbranch_vccz .Lcensus_2

.LBB0_590:
	s_or_b64 exec, exec, s[4:5]
	s_waitcnt lgkmcnt(0)
	s_mov_b32 s0, s98
	v_mbcnt_lo_u32_b32 v0, -1, 0
	v_mbcnt_hi_u32_b32 v0, -1, v0
	s_nop 1
	v_lshl_add_u32 v6, s0, 6, v0
	s_nop 0
	v_ashrrev_i32_e32 v0, 6, v6
	v_add_u32_e32 v0, -1, v0
	v_cmp_gt_u32_e32 vcc, 3, v0
	s_and_saveexec_b64 s[4:5], vcc
	s_cbranch_execz .LBB0_680
	s_lshl_b32 s0, s33, 1
	s_add_i32 s0, s0, s2
	v_mad_u64_u32 v[2:3], s[0:1], s0, 3, v[0:1]
	s_movk_i32 s0, 0x1d00
	s_nop 0
	v_cmp_gt_i32_e32 vcc, s0, v2
	s_and_b64 exec, exec, vcc
	s_cbranch_execz .LBB0_680
	s_movk_i32 s1, 0x1100
	s_movk_i32 s0, 0xbff
	v_mov_b32_e32 v1, 0xffffef00
	v_mov_b32_e32 v3, 0xfffff400
	v_cmp_gt_u32_e32 vcc, s1, v2
	v_mov_b32_e32 v4, 0x280
	s_nop 0
	v_cndmask_b32_e32 v1, v1, v3, vcc
	v_cndmask_b32_e64 v3, 2, 1, vcc
	v_cmp_lt_i32_e32 vcc, s0, v2
	s_nop 1
	v_cndmask_b32_e32 v1, v4, v1, vcc
	v_cndmask_b32_e32 v3, 0, v3, vcc
	v_add_u32_e32 v1, v1, v2
	v_cmp_lt_i32_e32 vcc, 0, v3
	s_and_saveexec_b64 s[0:1], vcc
	s_xor_b64 s[0:1], exec, s[0:1]
	s_cbranch_execz .LBB0_598
	v_cmp_ne_u32_e32 vcc, 1, v3
	s_and_saveexec_b64 s[8:9], vcc
	s_xor_b64 s[8:9], exec, s[8:9]
	s_movk_i32 s3, 0x800
	v_mov_b32_e32 v2, 0x1380
	v_mov_b32_e32 v3, 0xf80
	v_cmp_gt_i32_e32 vcc, s3, v1
	s_nop 1
	v_cndmask_b32_e32 v2, v2, v3, vcc
	v_add_u32_e32 v1, v2, v1
	s_andn2_saveexec_b64 s[8:9], s[8:9]
	v_add_u32_e32 v1, 0x280, v1
	s_or_b64 exec, exec, s[8:9]

.LBB0_680:
	s_or_b64 exec, exec, s[4:5]
	s_waitcnt lgkmcnt(0)
	s_mov_b32 s0, s98
	v_mbcnt_lo_u32_b32 v0, -1, 0
	v_mbcnt_hi_u32_b32 v0, -1, v0
	s_nop 1
	v_lshl_add_u32 v0, s0, 6, v0
	s_nop 0
	v_cmp_eq_u32_e32 vcc, 0, v0
	s_and_saveexec_b64 s[0:1], vcc
	s_cbranch_execz .LBB0_710
	s_add_i32 s3, 0, 0x24808
	v_mov_b32_e32 v0, s3
	s_add_i32 s3, 0, 0x2480c
	v_mov_b32_e32 v1, s3
	ds_read_b32 v0, v0
	ds_read_b32 v1, v1
	s_waitcnt lgkmcnt(0)
	v_cmp_eq_u32_e32 vcc, 0, v1
	s_cbranch_vccnz .LBB0_691
	v_mov_b32_e32 v1, 0x3000
	s_add_i32 s3, 0, 0x24804
	v_mov_b32_e32 v3, s3
	ds_read_b32 v3, v3
	global_load_dword v1, v1, s[94:95] offset:1024 sc1
	s_waitcnt lgkmcnt(0)
	v_mul_lo_u32 v0, v0, v3
	s_add_u32 s4, s94, 0x3400
	s_addc_u32 s5, s95, 0
	s_waitcnt vmcnt(0)
	v_cmp_ge_u32_e32 vcc, v1, v0
	s_cbranch_vccnz .LBB0_696
	s_mov_b32 s3, 1
	v_mov_b32_e32 v1, 0
	s_branch .LBB0_685

.LBB0_711:
	v_readlane_b32 s40, v249, 51
	s_cmp_lt_i32 s40, 5
	s_cselect_b64 s[8:9], -1, 0
	s_cmp_gt_i32 s40, 4
	s_cselect_b64 s[4:5], -1, 0
	s_and_b64 s[0:1], s[8:9], s[6:7]
	v_readlane_b32 s41, v249, 52
	s_andn2_b64 vcc, exec, s[0:1]
	v_readlane_b32 s42, v249, 53
	v_readlane_b32 s43, v249, 54
	s_cbranch_vccnz .LBB0_732
	s_cmpk_gt_i32 s2, 0xff
	s_waitcnt lgkmcnt(0)
	s_mov_b32 s0, s98
	v_mbcnt_lo_u32_b32 v0, -1, 0
	v_mbcnt_hi_u32_b32 v0, -1, v0
	s_nop 1
	v_lshl_add_u32 v0, s0, 6, v0
	s_nop 0
	v_readfirstlane_b32 s1, v0
	s_cbranch_scc1 .LBB0_732
	v_bfe_i32 v3, v0, 27, 1
	v_lshlrev_b32_e32 v1, 4, v0
	v_lshrrev_b32_e32 v3, 22, v3
	v_add_u32_e32 v3, v1, v3
	v_and_b32_e32 v3, 0xfffffc00, v3
	v_ashrrev_i32_e32 v2, 31, v0
	v_sub_u32_e32 v1, v1, v3
	v_lshrrev_b32_e32 v2, 26, v2
	v_lshrrev_b32_e32 v3, 4, v1
	v_add_u32_e32 v2, v0, v2
	v_bitop3_b32 v3, v3, v1, 32 bitop3:0x6c
	v_ashrrev_i32_e32 v1, 31, v1
	s_add_u32 s3, s78, 0x15500000
	v_ashrrev_i32_e32 v2, 6, v2
	v_lshrrev_b32_e32 v1, 26, v1
	s_addc_u32 s13, s79, 0
	v_lshlrev_b32_e32 v4, 3, v2
	v_add_u32_e32 v1, v3, v1
	s_add_u32 s34, s78, 0x1700000
	v_and_b32_e32 v4, -16, v4
	v_ashrrev_i32_e32 v1, 6, v1
	s_addc_u32 s35, s79, 0
	v_add_u32_e32 v4, v1, v4
	v_mul_i32_i24_e32 v5, 64, v1
	v_and_b32_e32 v1, 3, v1
	s_mov_b32 s0, 0x1fffe0
	s_ashr_i32 s37, s2, 31
	v_and_or_b32 v1, v4, s0, v1
	s_lshr_b32 s0, s37, 29
	s_add_i32 s0, s2, s0
	s_ashr_i32 s6, s0, 3
	s_and_b32 s0, s0, -8
	s_ashr_i32 s10, s1, 6
	s_sub_i32 s0, s2, s0
	s_ashr_i32 s11, s1, 8
	s_lshl_b32 s36, s10, 10
	s_lshl_b32 s12, s0, 5
	s_mul_i32 s7, s0, 33
	s_cmp_lt_i32 s0, 0
	s_cselect_b32 s0, s7, s12
	s_add_i32 s0, s0, s6
	s_ashr_i32 s6, s0, 31
	s_lshr_b32 s6, s6, 27
	s_add_i32 s6, s0, s6
	s_ashr_i32 s7, s6, 5
	s_andn2_b32 s6, s6, 31
	s_sub_i32 s6, s0, s6
	s_bfe_i32 s0, s6, 0x80000
	s_bfe_u32 s0, s0, 0x3000c
	s_add_i32 s12, s6, s0
	s_bfe_i32 s0, s12, 0x80000
	s_and_b32 s12, s12, 0xf8
	s_sub_i32 s6, s6, s12
	s_lshl_b32 s7, s7, 3
	s_sext_i32_i8 s6, s6
	s_add_i32 s22, s7, s6
	s_sext_i32_i16 s0, s0
	s_ashr_i32 s23, s22, 31
	s_lshr_b32 s0, s0, 3
	s_lshl_b64 s[6:7], s[22:23], 19
	v_sub_u32_e32 v3, v3, v5
	v_mov_b32_e32 v5, 1
	s_add_u32 s24, s3, s6
	v_lshlrev_b32_e32 v2, 5, v2
	v_ashrrev_i16_sdwa v3, v5, sext(v3) dst_sel:DWORD dst_unused:UNUSED_PAD src0_sel:DWORD src1_sel:BYTE_0
	v_lshlrev_b32_e32 v5, 1, v4
	v_lshrrev_b32_e32 v6, 2, v4
	s_addc_u32 s25, s13, s7
	s_bfe_i64 s[6:7], s[0:1], 0x100000
	v_and_b32_e32 v2, 32, v2
	v_bfe_i32 v3, v3, 0, 16
	v_and_b32_e32 v5, 24, v5
	v_and_b32_e32 v6, 4, v6
	s_lshl_b64 s[6:7], s[6:7], 19
	v_or3_b32 v1, v1, v6, v5
	v_add_lshl_u32 v2, v2, v3, 1
	s_add_u32 s26, s34, s6
	v_lshl_add_u32 v174, v1, 11, v2
	s_addc_u32 s27, s35, s7
	s_add_i32 s23, s36, 0
	s_mov_b64 s[6:7], s[26:27]
	s_add_i32 m0, s23, 0x10000
	v_lshl_add_u32 v175, v4, 11, v2
	global_load_lds_dwordx4 v174, s[6:7]
	s_add_u32 s6, s26, 0x20000
	s_addc_u32 s7, s27, 0
	s_add_i32 m0, s23, 0x12000
	s_nop 0
	global_load_lds_dwordx4 v174, s[6:7]
	s_add_i32 m0, s23, 0x14000
	s_add_u32 s6, s26, 0x40000
	s_addc_u32 s7, s27, 0
	s_nop 0
	global_load_lds_dwordx4 v174, s[6:7]
	s_add_u32 s6, s26, 0x60000
	s_addc_u32 s7, s27, 0
	s_add_i32 m0, s23, 0x16000
	s_nop 0
	global_load_lds_dwordx4 v174, s[6:7]
	s_mov_b64 s[6:7], s[24:25]
	s_mov_b32 m0, s23
	s_nop 0
	global_load_lds_dwordx4 v175, s[6:7]
	s_add_u32 s6, s24, 0x20000
	s_addc_u32 s7, s25, 0
	s_add_i32 s38, s23, 0x2000
	s_mov_b32 m0, s38
	s_add_i32 s39, s23, 0x4000
	global_load_lds_dwordx4 v175, s[6:7]
	s_add_u32 s6, s24, 0x40000
	s_addc_u32 s7, s25, 0
	s_mov_b32 m0, s39
	s_nop 0
	global_load_lds_dwordx4 v175, s[6:7]
	s_add_u32 s6, s24, 0x60000
	s_addc_u32 s7, s25, 0
	s_add_i32 s40, s23, 0x6000
	s_mov_b32 m0, s40
	s_cmp_eq_u32 s11, 1
	global_load_lds_dwordx4 v175, s[6:7]
	s_cselect_b64 s[6:7], -1, 0
	s_cmp_lg_u32 s11, 1
	s_cbranch_scc1 .LBB0_715
	s_barrier

.LBB0_732:
	s_cmp_gt_i32 s41, 5
	s_cselect_b64 s[12:13], -1, 0
	s_and_b64 s[0:1], s[8:9], s[12:13]
	s_andn2_b64 vcc, exec, s[0:1]
	s_cbranch_vccnz .LBB0_890
	s_waitcnt vmcnt(0)
	s_waitcnt lgkmcnt(0)
	s_barrier
	s_waitcnt lgkmcnt(0)
	s_mov_b32 s0, s98
	v_mbcnt_lo_u32_b32 v0, -1, 0
	v_mbcnt_hi_u32_b32 v0, -1, v0
	s_nop 1
	v_lshl_add_u32 v0, s0, 6, v0
	s_nop 0
	v_cmp_eq_u32_e32 vcc, 0, v0
	s_and_saveexec_b64 s[6:7], vcc
	s_cbranch_execz .LBB0_761
	s_add_i32 s0, 0, 0x24800
	v_mov_b32_e32 v0, s0
	s_waitcnt vmcnt(0) expcnt(0) lgkmcnt(0)
	ds_read_b32 v1, v0
	s_add_i32 s0, 0, 0x24804
	v_mov_b32_e32 v0, s0
	ds_read_b32 v0, v0
	s_waitcnt lgkmcnt(1)
	v_cmp_ne_u32_e32 vcc, 0, v1
	s_cbranch_vccz .Lcensus_3

.LBB0_761:
	s_or_b64 exec, exec, s[6:7]
	v_mbcnt_lo_u32_b32 v1, -1, 0
	v_mbcnt_hi_u32_b32 v1, -1, v1
	v_mov_b32_e32 v44, 0
	v_mov_b32_e32 v45, 0
	v_mov_b32_e32 v46, 0
	s_waitcnt lgkmcnt(0)
	s_mov_b32 s0, s98
	v_mov_b32_e32 v47, 0
	v_mov_b32_e32 v30, 0
	v_lshl_add_u32 v52, s0, 6, v1
	s_movk_i32 s0, 0x100
	v_ashrrev_i32_e32 v53, 31, v52
	v_lshl_add_u64 v[24:25], v[52:53], 4, s[78:79]
	v_add_co_u32_e32 v0, vcc, 0x1200000, v24
	v_cmp_gt_i32_e64 s[0:1], s0, v52
	s_nop 0
	v_addc_co_u32_e32 v1, vcc, 0, v25, vcc
	v_add_co_u32_e32 v4, vcc, 0x1202000, v24
	v_mov_b32_e32 v31, 0
	s_nop 0
	v_addc_co_u32_e32 v5, vcc, 0, v25, vcc
	v_add_co_u32_e32 v8, vcc, 0x1204000, v24
	global_load_dwordx4 v[0:3], v[0:1], off
	s_nop 0
	global_load_dwordx4 v[4:7], v[4:5], off
	v_addc_co_u32_e32 v9, vcc, 0, v25, vcc
	v_add_co_u32_e32 v12, vcc, 0x1206000, v24
	v_mov_b32_e32 v58, 0
	s_nop 0
	v_addc_co_u32_e32 v13, vcc, 0, v25, vcc
	v_add_co_u32_e32 v16, vcc, 0x1208000, v24
	global_load_dwordx4 v[8:11], v[8:9], off
	s_nop 0
	global_load_dwordx4 v[12:15], v[12:13], off
	v_addc_co_u32_e32 v17, vcc, 0, v25, vcc
	v_add_co_u32_e32 v20, vcc, 0x120a000, v24
	v_mov_b32_e32 v59, 0
	s_nop 0
	v_addc_co_u32_e32 v21, vcc, 0, v25, vcc
	v_add_co_u32_e32 v26, vcc, 0x120c000, v24
	global_load_dwordx4 v[16:19], v[16:17], off
	s_nop 0
	global_load_dwordx4 v[20:23], v[20:21], off
	v_addc_co_u32_e32 v27, vcc, 0, v25, vcc
	v_add_co_u32_e32 v28, vcc, 0x120e000, v24
	v_mov_b32_e32 v60, 0
	s_nop 0
	v_addc_co_u32_e32 v29, vcc, 0, v25, vcc
	v_add_co_u32_e32 v24, vcc, 0x1210000, v24
	global_load_dwordx4 v[32:35], v[26:27], off
	global_load_dwordx4 v[36:39], v[28:29], off
	v_addc_co_u32_e32 v25, vcc, 0, v25, vcc
	global_load_dwordx4 v[40:43], v[24:25], off
	v_mov_b32_e32 v28, 0
	v_mov_b32_e32 v29, 0
	v_mov_b32_e32 v24, 0
	v_mov_b32_e32 v25, 0
	v_mov_b32_e32 v26, 0
	v_mov_b32_e32 v27, 0
	v_mov_b32_e32 v61, 0
	v_mov_b32_e32 v54, 0
	v_mov_b32_e32 v55, 0
	v_mov_b32_e32 v56, 0
	v_mov_b32_e32 v57, 0
	v_mov_b32_e32 v48, 0
	v_mov_b32_e32 v49, 0
	v_mov_b32_e32 v50, 0
	v_mov_b32_e32 v51, 0
	s_and_saveexec_b64 s[6:7], s[0:1]
	s_cbranch_execz .LBB0_763
	v_lshlrev_b32_e32 v24, 2, v52
	v_readlane_b32 s16, v249, 2
	v_ashrrev_i32_e32 v25, 31, v24
	v_readlane_b32 s26, v249, 12
	v_readlane_b32 s27, v249, 13
	v_lshlrev_b64 v[44:45], 2, v[24:25]
	v_readlane_b32 s17, v249, 3
	v_readlane_b32 s18, v249, 4
	v_readlane_b32 s19, v249, 5
	v_readlane_b32 s28, v249, 14
	v_readlane_b32 s29, v249, 15
	s_mov_b64 s[14:15], s[26:27]
	v_readlane_b32 s30, v249, 16
	v_readlane_b32 s31, v249, 17
	s_mov_b64 s[16:17], s[28:29]
	v_lshl_add_u64 v[24:25], s[14:15], 0, v[44:45]
	global_load_dwordx4 v[28:31], v[24:25], off
	v_lshl_add_u64 v[24:25], s[16:17], 0, v[44:45]
	v_lshl_add_u64 v[44:45], s[78:79], 0, v[44:45]
	v_add_co_u32_e32 v46, vcc, 0x44000, v44
	global_load_dwordx4 v[24:27], v[24:25], off
	s_nop 0
	v_addc_co_u32_e32 v47, vcc, 0, v45, vcc
	v_add_co_u32_e32 v48, vcc, 0x43000, v44
	v_readlane_b32 s20, v249, 6
	s_nop 0
	v_addc_co_u32_e32 v49, vcc, 0, v45, vcc
	global_load_dwordx4 v[54:57], v[46:47], off
	s_nop 0
	global_load_dwordx4 v[48:51], v[48:49], off
	v_add_co_u32_e32 v46, vcc, 0x4a000, v44
	v_readlane_b32 s21, v249, 7
	s_nop 0
	v_addc_co_u32_e32 v47, vcc, 0, v45, vcc
	v_add_co_u32_e32 v44, vcc, 0x49000, v44
	global_load_dwordx4 v[62:65], v[46:47], off
	s_nop 0
	v_addc_co_u32_e32 v45, vcc, 0, v45, vcc
	global_load_dwordx4 v[44:47], v[44:45], off
	v_readlane_b32 s22, v249, 8
	v_readlane_b32 s23, v249, 9
	v_readlane_b32 s24, v249, 10
	v_readlane_b32 s25, v249, 11
	s_mov_b64 s[18:19], s[30:31]
	s_waitcnt vmcnt(3)
	v_pk_add_f32 v[60:61], v[56:57], 1.0 op_sel_hi:[1,0]
	v_pk_add_f32 v[58:59], v[54:55], 1.0 op_sel_hi:[1,0]
	s_waitcnt vmcnt(1)
	v_pk_add_f32 v[56:57], v[64:65], 1.0 op_sel_hi:[1,0]
	v_pk_add_f32 v[54:55], v[62:63], 1.0 op_sel_hi:[1,0]

.LBB0_767:
	s_or_b64 exec, exec, s[6:7]
	s_waitcnt lgkmcnt(0)
	s_barrier
	s_waitcnt lgkmcnt(0)
	s_mov_b32 s0, s98
	v_mbcnt_lo_u32_b32 v0, -1, 0
	v_mbcnt_hi_u32_b32 v0, -1, v0
	s_nop 1
	v_lshl_add_u32 v6, s0, 6, v0
	s_nop 0
	v_ashrrev_i32_e32 v0, 6, v6
	v_add_u32_e32 v0, -1, v0
	v_cmp_gt_u32_e32 vcc, 3, v0
	s_and_saveexec_b64 s[6:7], vcc
	s_cbranch_execz .LBB0_857
	s_mul_i32 s0, s33, 3
	s_add_i32 s0, s0, s2
	v_mad_u64_u32 v[2:3], s[0:1], s0, 3, v[0:1]
	s_movk_i32 s0, 0x1d00
	s_nop 0
	v_cmp_gt_i32_e32 vcc, s0, v2
	s_and_b64 exec, exec, vcc
	s_cbranch_execz .LBB0_857
	s_movk_i32 s1, 0x1100
	s_movk_i32 s0, 0xbff
	v_mov_b32_e32 v1, 0xffffef00
	v_mov_b32_e32 v3, 0xfffff400
	v_cmp_gt_u32_e32 vcc, s1, v2
	v_mov_b32_e32 v4, 0x280
	s_nop 0
	v_cndmask_b32_e32 v1, v1, v3, vcc
	v_cndmask_b32_e64 v3, 2, 1, vcc
	v_cmp_lt_i32_e32 vcc, s0, v2
	s_nop 1
	v_cndmask_b32_e32 v1, v4, v1, vcc
	v_cndmask_b32_e32 v3, 0, v3, vcc
	v_add_u32_e32 v1, v1, v2
	v_cmp_lt_i32_e32 vcc, 0, v3
	s_and_saveexec_b64 s[0:1], vcc
	s_xor_b64 s[0:1], exec, s[0:1]
	s_cbranch_execz .LBB0_775
	v_cmp_ne_u32_e32 vcc, 1, v3
	s_and_saveexec_b64 s[8:9], vcc
	s_xor_b64 s[8:9], exec, s[8:9]
	s_movk_i32 s3, 0x800
	v_mov_b32_e32 v2, 0x1380
	v_mov_b32_e32 v3, 0xf80
	v_cmp_gt_i32_e32 vcc, s3, v1
	s_nop 1
	v_cndmask_b32_e32 v2, v2, v3, vcc
	v_add_u32_e32 v1, v2, v1
	s_andn2_saveexec_b64 s[8:9], s[8:9]
	v_add_u32_e32 v1, 0x280, v1
	s_or_b64 exec, exec, s[8:9]

.LBB0_890:
	s_add_u32 s8, s78, 0xa500000
	s_addc_u32 s9, s79, 0
	s_add_u32 s6, s78, 0xa00000
	s_addc_u32 s7, s79, 0
	s_add_u32 s10, s78, 0xe00000
	s_addc_u32 s11, s79, 0
	s_cmp_lt_i32 s40, 6
	s_cselect_b64 s[14:15], -1, 0
	s_and_b64 s[0:1], s[14:15], s[12:13]
	s_andn2_b64 vcc, exec, s[0:1]
	s_cbranch_vccnz .LBB0_923
	v_mbcnt_lo_u32_b32 v1, -1, 0
	v_mbcnt_hi_u32_b32 v1, -1, v1
	s_lshl_b32 s0, s2, 5
	v_mov_b32_e32 v87, 0
	s_andn2_b64 vcc, exec, s[4:5]
	s_waitcnt lgkmcnt(0)
	s_mov_b32 s1, s98
	s_nop 1
	v_lshl_add_u32 v114, s1, 6, v1
	s_nop 0
	v_ashrrev_i32_e32 v97, 6, v114
	v_bfe_u32 v115, v114, 4, 2
	v_and_b32_e32 v98, 15, v114
	v_lshl_add_u32 v96, v97, 2, s0
	v_or_b32_e32 v0, v96, v115
	v_lshlrev_b32_e32 v116, 3, v98
	v_lshl_or_b32 v86, v0, 10, v116
	v_lshl_add_u64 v[0:1], v[86:87], 1, s[76:77]
	global_load_dwordx4 v[60:63], v[0:1], off nt
	global_load_dwordx4 v[56:59], v[0:1], off offset:256 nt
	global_load_dwordx4 v[52:55], v[0:1], off offset:512 nt
	global_load_dwordx4 v[48:51], v[0:1], off offset:768 nt
	global_load_dwordx4 v[44:47], v[0:1], off offset:1024 nt
	global_load_dwordx4 v[40:43], v[0:1], off offset:1280 nt
	global_load_dwordx4 v[36:39], v[0:1], off offset:1536 nt
	global_load_dwordx4 v[32:35], v[0:1], off offset:1792 nt
	s_cbranch_vccnz .LBB0_899
	v_mbcnt_lo_u32_b32 v1, -1, 0
	v_mbcnt_hi_u32_b32 v1, -1, v1
	v_mov_b32_e32 v77, 0
	v_mov_b32_e32 v78, 0
	v_mov_b32_e32 v79, 0
	s_waitcnt lgkmcnt(0)
	s_mov_b32 s0, s98
	v_mov_b32_e32 v30, 0
	v_mov_b32_e32 v31, 0
	v_lshl_add_u32 v84, s0, 6, v1
	s_movk_i32 s0, 0x100
	v_ashrrev_i32_e32 v85, 31, v84
	v_lshl_add_u64 v[20:21], v[84:85], 4, s[78:79]
	v_add_co_u32_e32 v0, vcc, 0x1200000, v20
	v_cmp_gt_i32_e64 s[0:1], s0, v84
	s_nop 0
	v_addc_co_u32_e32 v1, vcc, 0, v21, vcc
	v_add_co_u32_e32 v4, vcc, 0x1202000, v20
	v_mov_b32_e32 v92, 0
	s_nop 0
	v_addc_co_u32_e32 v5, vcc, 0, v21, vcc
	v_add_co_u32_e32 v8, vcc, 0x1204000, v20
	global_load_dwordx4 v[0:3], v[0:1], off
	s_nop 0
	global_load_dwordx4 v[4:7], v[4:5], off
	v_addc_co_u32_e32 v9, vcc, 0, v21, vcc
	v_add_co_u32_e32 v12, vcc, 0x1206000, v20
	v_mov_b32_e32 v93, 0
	s_nop 0
	v_addc_co_u32_e32 v13, vcc, 0, v21, vcc
	v_add_co_u32_e32 v16, vcc, 0x1208000, v20
	global_load_dwordx4 v[8:11], v[8:9], off
	s_nop 0
	global_load_dwordx4 v[12:15], v[12:13], off
	v_addc_co_u32_e32 v17, vcc, 0, v21, vcc
	v_add_co_u32_e32 v22, vcc, 0x120a000, v20
	v_mov_b32_e32 v94, 0
	s_nop 0
	v_addc_co_u32_e32 v23, vcc, 0, v21, vcc
	global_load_dwordx4 v[16:19], v[16:17], off
	s_nop 0
	global_load_dwordx4 v[24:27], v[22:23], off
	v_add_co_u32_e32 v22, vcc, 0x120c000, v20
	v_mov_b32_e32 v95, 0
	s_nop 0
	v_addc_co_u32_e32 v23, vcc, 0, v21, vcc
	v_add_co_u32_e32 v28, vcc, 0x120e000, v20
	v_mov_b32_e32 v88, 0
	s_nop 0
	v_addc_co_u32_e32 v29, vcc, 0, v21, vcc
	v_add_co_u32_e32 v20, vcc, 0x1210000, v20
	global_load_dwordx4 v[64:67], v[22:23], off
	global_load_dwordx4 v[68:71], v[28:29], off
	v_addc_co_u32_e32 v21, vcc, 0, v21, vcc
	global_load_dwordx4 v[72:75], v[20:21], off
	v_mov_b32_e32 v28, 0
	v_mov_b32_e32 v29, 0
	v_mov_b32_e32 v20, 0
	v_mov_b32_e32 v21, 0
	v_mov_b32_e32 v22, 0
	v_mov_b32_e32 v23, 0
	v_mov_b32_e32 v89, 0
	v_mov_b32_e32 v90, 0
	v_mov_b32_e32 v91, 0
	v_mov_b32_e32 v80, 0
	v_mov_b32_e32 v81, 0
	v_mov_b32_e32 v82, 0
	v_mov_b32_e32 v83, 0
	s_and_saveexec_b64 s[4:5], s[0:1]
	s_cbranch_execz .LBB0_894
	v_lshlrev_b32_e32 v20, 2, v84
	v_readlane_b32 s16, v249, 2
	v_ashrrev_i32_e32 v21, 31, v20
	v_readlane_b32 s18, v249, 4
	v_readlane_b32 s19, v249, 5
	v_readlane_b32 s26, v249, 12
	v_readlane_b32 s27, v249, 13
	v_lshlrev_b64 v[76:77], 2, v[20:21]
	v_readlane_b32 s20, v249, 6
	v_readlane_b32 s21, v249, 7
	v_readlane_b32 s22, v249, 8
	v_readlane_b32 s23, v249, 9
	v_readlane_b32 s28, v249, 14
	v_readlane_b32 s29, v249, 15
	s_mov_b64 s[18:19], s[26:27]
	v_readlane_b32 s30, v249, 16
	v_readlane_b32 s31, v249, 17
	s_mov_b64 s[20:21], s[28:29]
	v_lshl_add_u64 v[20:21], s[18:19], 0, v[76:77]
	global_load_dwordx4 v[28:31], v[20:21], off
	v_lshl_add_u64 v[20:21], s[20:21], 0, v[76:77]
	v_lshl_add_u64 v[76:77], s[78:79], 0, v[76:77]
	v_add_co_u32_e32 v78, vcc, 0x44000, v76
	global_load_dwordx4 v[20:23], v[20:21], off
	s_nop 0
	v_addc_co_u32_e32 v79, vcc, 0, v77, vcc
	v_add_co_u32_e32 v80, vcc, 0x43000, v76
	global_load_dwordx4 v[86:89], v[78:79], off
	s_nop 0
	v_addc_co_u32_e32 v81, vcc, 0, v77, vcc
	v_add_co_u32_e32 v78, vcc, 0x4a000, v76
	v_readlane_b32 s17, v249, 3
	s_nop 0
	v_addc_co_u32_e32 v79, vcc, 0, v77, vcc
	v_add_co_u32_e32 v76, vcc, 0x49000, v76
	global_load_dwordx4 v[100:103], v[78:79], off
	s_nop 0
	v_addc_co_u32_e32 v77, vcc, 0, v77, vcc
	global_load_dwordx4 v[76:79], v[76:77], off
	s_nop 0
	global_load_dwordx4 v[80:83], v[80:81], off
	v_readlane_b32 s24, v249, 10
	v_readlane_b32 s25, v249, 11
	s_mov_b64 s[22:23], s[30:31]
	s_waitcnt vmcnt(3)
	v_pk_add_f32 v[94:95], v[88:89], 1.0 op_sel_hi:[1,0]
	v_pk_add_f32 v[92:93], v[86:87], 1.0 op_sel_hi:[1,0]
	s_waitcnt vmcnt(2)
	v_pk_add_f32 v[90:91], v[102:103], 1.0 op_sel_hi:[1,0]
	v_pk_add_f32 v[88:89], v[100:101], 1.0 op_sel_hi:[1,0]
	s_waitcnt vmcnt(1)
	v_mov_b32_e32 v87, v76

.LBB0_923:
	s_cmp_gt_i32 s41, 6
	s_cselect_b64 s[4:5], -1, 0
	s_and_b64 s[0:1], s[14:15], s[4:5]
	s_andn2_b64 vcc, exec, s[0:1]
	s_cbranch_vccnz .LBB0_1075
	s_waitcnt vmcnt(0)
	s_waitcnt lgkmcnt(0)
	s_barrier
	s_waitcnt lgkmcnt(0)
	s_mov_b32 s0, s98
	v_mbcnt_lo_u32_b32 v0, -1, 0
	v_mbcnt_hi_u32_b32 v0, -1, v0
	s_nop 1
	v_lshl_add_u32 v0, s0, 6, v0
	s_nop 0
	v_cmp_eq_u32_e32 vcc, 0, v0
	s_and_saveexec_b64 s[12:13], vcc
	s_cbranch_execz .LBB0_954
	s_add_i32 s0, 0, 0x24800
	v_mov_b32_e32 v0, s0
	s_waitcnt vmcnt(0) expcnt(0) lgkmcnt(0)
	ds_read_b32 v1, v0
	s_add_i32 s0, 0, 0x24804
	v_mov_b32_e32 v0, s0
	ds_read_b32 v0, v0
	s_waitcnt lgkmcnt(1)
	v_cmp_ne_u32_e32 vcc, 0, v1
	s_cbranch_vccz .Lcensus_4

.LBB0_954:
	s_or_b64 exec, exec, s[12:13]
	s_waitcnt lgkmcnt(0)
	s_mov_b32 s0, s98
	v_mbcnt_lo_u32_b32 v0, -1, 0
	v_mbcnt_hi_u32_b32 v0, -1, v0
	s_nop 1
	v_lshl_add_u32 v6, s0, 6, v0
	s_nop 0
	v_ashrrev_i32_e32 v0, 6, v6
	v_add_u32_e32 v0, -1, v0
	v_cmp_gt_u32_e32 vcc, 3, v0
	s_and_saveexec_b64 s[12:13], vcc
	s_cbranch_execz .LBB0_1044
	s_lshl_b32 s0, s33, 2
	s_add_i32 s0, s0, s2
	v_mad_u64_u32 v[2:3], s[0:1], s0, 3, v[0:1]
	s_movk_i32 s0, 0x1d00
	s_nop 0
	v_cmp_gt_i32_e32 vcc, s0, v2
	s_and_b64 exec, exec, vcc
	s_cbranch_execz .LBB0_1044
	s_movk_i32 s1, 0x1100
	s_movk_i32 s0, 0xbff
	v_mov_b32_e32 v1, 0xffffef00
	v_mov_b32_e32 v3, 0xfffff400
	v_cmp_gt_u32_e32 vcc, s1, v2
	v_mov_b32_e32 v4, 0x280
	s_nop 0
	v_cndmask_b32_e32 v1, v1, v3, vcc
	v_cndmask_b32_e64 v3, 2, 1, vcc
	v_cmp_lt_i32_e32 vcc, s0, v2
	s_nop 1
	v_cndmask_b32_e32 v1, v4, v1, vcc
	v_cndmask_b32_e32 v3, 0, v3, vcc
	v_add_u32_e32 v1, v1, v2
	v_cmp_lt_i32_e32 vcc, 0, v3
	s_and_saveexec_b64 s[0:1], vcc
	s_xor_b64 s[0:1], exec, s[0:1]
	s_cbranch_execz .LBB0_962
	v_cmp_ne_u32_e32 vcc, 1, v3
	s_and_saveexec_b64 s[14:15], vcc
	s_xor_b64 s[14:15], exec, s[14:15]
	s_movk_i32 s3, 0x800
	v_mov_b32_e32 v2, 0x1380
	v_mov_b32_e32 v3, 0xf80
	v_cmp_gt_i32_e32 vcc, s3, v1
	s_nop 1
	v_cndmask_b32_e32 v2, v2, v3, vcc
	v_add_u32_e32 v1, v2, v1
	s_andn2_saveexec_b64 s[14:15], s[14:15]
	v_add_u32_e32 v1, 0x280, v1
	s_or_b64 exec, exec, s[14:15]

.LBB0_1044:
	s_or_b64 exec, exec, s[12:13]
	s_waitcnt lgkmcnt(0)
	s_mov_b32 s0, s98
	v_mbcnt_lo_u32_b32 v0, -1, 0
	v_mbcnt_hi_u32_b32 v0, -1, v0
	s_nop 1
	v_lshl_add_u32 v0, s0, 6, v0
	s_nop 0
	v_cmp_eq_u32_e32 vcc, 0, v0
	s_and_saveexec_b64 s[0:1], vcc
	s_cbranch_execz .LBB0_1074
	s_add_i32 s3, 0, 0x24808
	v_mov_b32_e32 v0, s3
	s_add_i32 s3, 0, 0x2480c
	v_mov_b32_e32 v1, s3
	ds_read_b32 v0, v0
	ds_read_b32 v1, v1
	s_waitcnt lgkmcnt(0)
	v_cmp_eq_u32_e32 vcc, 0, v1
	s_cbranch_vccnz .LBB0_1055
	v_mov_b32_e32 v1, 0x3000
	s_add_i32 s3, 0, 0x24804
	v_mov_b32_e32 v3, s3
	ds_read_b32 v3, v3
	global_load_dword v1, v1, s[94:95] offset:1024 sc1
	s_waitcnt lgkmcnt(0)
	v_mul_lo_u32 v0, v0, v3
	s_add_u32 s12, s94, 0x3400
	s_addc_u32 s13, s95, 0
	s_waitcnt vmcnt(0)
	v_cmp_ge_u32_e32 vcc, v1, v0
	s_cbranch_vccnz .LBB0_1060
	s_mov_b32 s3, 1
	v_mov_b32_e32 v1, 0
	s_branch .LBB0_1049

.LBB0_1075:
	s_cmp_lt_i32 s40, 7
	s_cselect_b64 s[0:1], -1, 0
	s_and_b64 s[0:1], s[0:1], s[4:5]
	s_andn2_b64 vcc, exec, s[0:1]
	s_cbranch_vccnz .LBB0_1440
	s_waitcnt lgkmcnt(0)
	s_mov_b32 s0, s98
	v_mbcnt_lo_u32_b32 v0, -1, 0
	v_mbcnt_hi_u32_b32 v0, -1, v0
	s_nop 1
	v_lshl_add_u32 v2, s0, 6, v0
	s_nop 0
	v_cmp_gt_i32_e32 vcc, 64, v2
	s_and_saveexec_b64 s[4:5], vcc
	s_cbranch_execz .LBB0_1095
	v_cmp_gt_i32_e32 vcc, 32, v2
	v_mov_b32_e32 v0, 0
	s_and_saveexec_b64 s[0:1], vcc
	s_cbranch_execz .LBB0_1079
	v_lshlrev_b32_e32 v0, 6, v2
	v_ashrrev_i32_e32 v1, 31, v0
	v_lshl_add_u64 v[0:1], v[0:1], 2, s[78:79]
	global_load_dword v0, v[0:1], off

.LBB0_1095:
	s_or_b64 exec, exec, s[4:5]
	s_add_i32 s3, 0, 0x24000
	v_mov_b32_e32 v0, s3
	s_waitcnt lgkmcnt(0)
	s_barrier
	ds_read_b32 v0, v0
	s_and_b32 s5, s33, 7
	s_waitcnt lgkmcnt(0)
	v_readfirstlane_b32 s4, v0
	v_mbcnt_lo_u32_b32 v0, -1, 0
	v_mbcnt_hi_u32_b32 v0, -1, v0
	s_cmp_eq_u32 s5, 0
	s_waitcnt lgkmcnt(0)
	s_mov_b32 s0, s98
	s_mov_b32 s16, s2
	s_nop 0
	v_lshl_add_u32 v8, s0, 6, v0
	s_cselect_b64 s[0:1], -1, 0
	v_readfirstlane_b32 s18, v8
	s_cmp_lg_u32 s5, 0
	s_cbranch_scc1 .LBB0_1097
	s_and_b32 s5, s2, 7
	s_ashr_i32 s12, s33, 3
	s_mul_i32 s5, s12, s5
	s_ashr_i32 s12, s2, 3
	s_add_i32 s16, s5, s12

.LBB0_1278:
	v_mov_b32_e32 v1, s3
	v_mbcnt_lo_u32_b32 v2, -1, 0
	v_mbcnt_hi_u32_b32 v2, -1, v2
	s_waitcnt lgkmcnt(0)
	s_mov_b32 s0, s98
	s_nop 1
	v_lshl_add_u32 v6, s0, 6, v2
	ds_read_b32 v0, v1
	s_ashr_i32 s0, s2, 1
	s_add_i32 s15, s30, s0
	v_readfirstlane_b32 s22, v6
	s_waitcnt lgkmcnt(0)
	v_lshlrev_b32_e32 v0, 1, v0
	v_cmp_ge_i32_e32 vcc, s15, v0
	s_cbranch_vccnz .LBB0_1365
	s_and_b32 s0, s22, 0xffffffc0
	v_mbcnt_lo_u32_b32 v0, -1, 0
	v_mbcnt_hi_u32_b32 v0, -1, v0
	s_ashr_i32 s18, s15, 1
	v_add_u32_e32 v0, s0, v0
	s_lshl_b32 s0, s18, 2
	v_ashrrev_i32_e32 v2, 31, v0
	v_lshrrev_b32_e32 v2, 26, v2
	v_add_u32_e32 v2, v0, v2
	v_lshlrev_b32_e32 v1, 4, v0
	v_ashrrev_i32_e32 v2, 6, v2
	v_bfe_i32 v0, v0, 27, 1
	v_lshrrev_b32_e32 v0, 22, v0
	v_lshlrev_b32_e32 v2, 3, v2
	s_add_i32 s0, s3, s0
	v_add_u32_e32 v0, v1, v0
	v_and_b32_e32 v4, -16, v2
	v_mov_b32_e32 v2, s0
	v_and_b32_e32 v0, 0xfffffc00, v0
	ds_read2_b32 v[2:3], v2 offset0:64 offset1:224
	v_sub_u32_e32 v0, v1, v0
	v_lshrrev_b32_e32 v1, 4, v0
	v_ashrrev_i32_e32 v5, 31, v0
	v_and_b32_e32 v1, 32, v1
	v_lshrrev_b32_e32 v5, 26, v5
	v_xad_u32 v0, v1, v0, v5
	v_ashrrev_i32_e32 v5, 6, v0
	s_waitcnt lgkmcnt(0)
	v_ashrrev_i32_e32 v1, 31, v2
	v_mov_b32_e32 v0, v2
	v_lshlrev_b32_e32 v2, 2, v2
	v_add_u32_e32 v2, s3, v2
	ds_read_b32 v9, v2 offset:4
	s_and_b32 s20, s2, 1
	s_lshl_b32 s0, s20, 7
	v_add_u32_e32 v2, s0, v3
	v_add3_u32 v4, v2, v4, v5
	v_lshlrev_b64 v[2:3], 16, v[0:1]
	v_lshl_add_u64 v[2:3], s[6:7], 0, v[2:3]
	s_waitcnt lgkmcnt(0)
	v_cmp_lt_i32_e32 vcc, v4, v9
	v_mov_b32_e32 v7, 0
	v_mov_b32_e32 v8, 0
	s_and_saveexec_b64 s[0:1], vcc
	s_cbranch_execz .LBB0_1281
	v_ashrrev_i32_e32 v5, 31, v4
	v_lshl_add_u64 v[10:11], v[4:5], 2, v[2:3]
	global_load_dword v5, v[10:11], off
	s_waitcnt vmcnt(0)
	v_lshlrev_b32_e32 v5, 9, v5
	v_and_b32_e32 v8, 0x3fffc00, v5

.LBB0_1365:
	s_sub_i32 s0, s28, s30
	s_ashr_i32 s26, s30, 1
	s_lshl_b32 s27, s0, 1
	s_cmp_ge_i32 s2, s27
	s_waitcnt lgkmcnt(0)
	s_mov_b32 s0, s98
	v_mbcnt_lo_u32_b32 v1, -1, 0
	v_mbcnt_hi_u32_b32 v1, -1, v1
	s_nop 1
	v_lshl_add_u32 v0, s0, 6, v1
	s_cselect_b64 s[0:1], -1, 0
	s_and_b64 vcc, exec, s[0:1]
	v_readfirstlane_b32 s21, v0
	s_cbranch_vccz .LBB0_1368
	s_sub_i32 s14, s2, s27
	s_lshl_b32 s4, s26, 2
	s_mov_b64 s[10:11], 0
	s_cmp_ge_i32 s14, s4
	s_mov_b64 s[4:5], 0
	s_cbranch_scc1 .LBB0_1369
	s_and_b32 s38, s14, 3
	s_ashr_i32 s40, s14, 2
	s_mov_b64 s[4:5], -1
	s_branch .LBB0_1369

.LBB0_1440:
	v_readlane_b32 s48, v249, 51
	v_readlane_b32 s49, v249, 52
	s_cmp_lt_i32 s48, 8
	s_cselect_b64 s[0:1], -1, 0
	s_cmp_gt_i32 s49, 8
	s_cselect_b64 s[4:5], -1, 0
	s_and_b64 s[0:1], s[0:1], s[4:5]
	s_andn2_b64 vcc, exec, s[0:1]
	v_readlane_b32 s50, v249, 53
	v_readlane_b32 s51, v249, 54
	s_cbranch_vccnz .LBB0_1590
	s_waitcnt vmcnt(0)
	s_waitcnt vmcnt(0) lgkmcnt(0)
	s_barrier
	s_waitcnt lgkmcnt(0)
	s_mov_b32 s0, s98
	v_mbcnt_lo_u32_b32 v0, -1, 0
	v_mbcnt_hi_u32_b32 v0, -1, v0
	s_nop 1
	v_lshl_add_u32 v0, s0, 6, v0
	s_nop 0
	v_cmp_eq_u32_e32 vcc, 0, v0
	s_and_saveexec_b64 s[6:7], vcc
	s_cbranch_execz .LBB0_1469
	s_add_i32 s0, 0, 0x24800
	v_mov_b32_e32 v0, s0
	s_waitcnt vmcnt(0) expcnt(0) lgkmcnt(0)
	ds_read_b32 v1, v0
	s_add_i32 s0, 0, 0x24804
	v_mov_b32_e32 v0, s0
	ds_read_b32 v0, v0
	s_waitcnt lgkmcnt(1)
	v_cmp_ne_u32_e32 vcc, 0, v1
	s_cbranch_vccz .Lcensus_5

.LBB0_1469:
	s_or_b64 exec, exec, s[6:7]
	s_waitcnt lgkmcnt(0)
	s_mov_b32 s0, s98
	v_mbcnt_lo_u32_b32 v0, -1, 0
	v_mbcnt_hi_u32_b32 v0, -1, v0
	s_nop 1
	v_lshl_add_u32 v6, s0, 6, v0
	s_nop 0
	v_ashrrev_i32_e32 v0, 6, v6
	v_add_u32_e32 v0, -1, v0
	v_cmp_gt_u32_e32 vcc, 3, v0
	s_and_saveexec_b64 s[6:7], vcc
	s_cbranch_execz .LBB0_1559
	s_mul_i32 s0, s33, 5
	s_add_i32 s0, s0, s2
	v_mad_u64_u32 v[2:3], s[0:1], s0, 3, v[0:1]
	s_movk_i32 s0, 0x1d00
	s_nop 0
	v_cmp_gt_i32_e32 vcc, s0, v2
	s_and_b64 exec, exec, vcc
	s_cbranch_execz .LBB0_1559
	s_movk_i32 s1, 0x1100
	s_movk_i32 s0, 0xbff
	v_mov_b32_e32 v1, 0xffffef00
	v_mov_b32_e32 v3, 0xfffff400
	v_cmp_gt_u32_e32 vcc, s1, v2
	v_mov_b32_e32 v4, 0x280
	s_nop 0
	v_cndmask_b32_e32 v1, v1, v3, vcc
	v_cndmask_b32_e64 v3, 2, 1, vcc
	v_cmp_lt_i32_e32 vcc, s0, v2
	s_nop 1
	v_cndmask_b32_e32 v1, v4, v1, vcc
	v_cndmask_b32_e32 v3, 0, v3, vcc
	v_add_u32_e32 v1, v1, v2
	v_cmp_lt_i32_e32 vcc, 0, v3
	s_and_saveexec_b64 s[0:1], vcc
	s_xor_b64 s[0:1], exec, s[0:1]
	s_cbranch_execz .LBB0_1477
	v_cmp_ne_u32_e32 vcc, 1, v3
	s_and_saveexec_b64 s[10:11], vcc
	s_xor_b64 s[10:11], exec, s[10:11]
	s_movk_i32 s3, 0x800
	v_mov_b32_e32 v2, 0x1380
	v_mov_b32_e32 v3, 0xf80
	v_cmp_gt_i32_e32 vcc, s3, v1
	s_nop 1
	v_cndmask_b32_e32 v2, v2, v3, vcc
	v_add_u32_e32 v1, v2, v1
	s_andn2_saveexec_b64 s[10:11], s[10:11]
	v_add_u32_e32 v1, 0x280, v1
	s_or_b64 exec, exec, s[10:11]

.LBB0_1590:
	s_cmp_lt_i32 s48, 9
	s_cselect_b64 s[6:7], -1, 0
	s_and_b64 s[0:1], s[6:7], s[4:5]
	s_andn2_b64 vcc, exec, s[0:1]
	s_cbranch_vccnz .LBB0_1603
	v_mbcnt_lo_u32_b32 v1, -1, 0
	v_mbcnt_hi_u32_b32 v1, -1, v1
	s_lshl_b32 s0, s2, 3
	s_movk_i32 s3, 0x4000
	s_waitcnt lgkmcnt(0)
	s_mov_b32 s1, s98
	s_nop 1
	v_lshl_add_u32 v1, s1, 6, v1
	s_nop 0
	v_ashrrev_i32_e32 v0, 6, v1
	v_add_u32_e32 v21, s0, v0
	v_cmp_gt_i32_e32 vcc, s3, v21
	s_and_saveexec_b64 s[10:11], vcc
	s_cbranch_execz .LBB0_1602
	v_readlane_b32 s52, v249, 2
	v_readlane_b32 s62, v249, 12
	v_readlane_b32 s63, v249, 13
	s_lshl_b32 s31, s33, 3
	s_lshl_b32 s12, s33, 4
	s_mov_b64 s[18:19], s[62:63]
	v_readlane_b32 s64, v249, 14
	v_readlane_b32 s65, v249, 15
	s_add_u32 s4, s18, 0x1000
	v_readlane_b32 s66, v249, 16
	v_readlane_b32 s67, v249, 17
	s_mov_b64 s[20:21], s[64:65]
	s_addc_u32 s5, s19, 0
	v_lshlrev_b32_e32 v2, 3, v1
	s_add_u32 s16, s20, 0x1000
	v_and_b32_e32 v16, 0x1f8, v2
	v_and_b32_e32 v1, 63, v1
	s_addc_u32 s17, s21, 0
	v_mov_b32_e32 v19, 0
	v_or_b32_e32 v20, 0x200, v16
	v_lshlrev_b32_e32 v18, 2, v16
	s_waitcnt vmcnt(0)
	v_lshlrev_b32_e32 v34, 4, v1
	v_ashrrev_i32_e32 v1, 31, v0
	s_ashr_i32 s1, s0, 31
	v_mov_b32_e32 v17, v19
	v_lshl_add_u64 v[22:23], s[4:5], 0, v[18:19]
	v_lshl_add_u64 v[24:25], s[16:17], 0, v[18:19]
	v_lshlrev_b32_e32 v18, 2, v20
	v_lshl_add_u64 v[0:1], v[0:1], 0, s[0:1]
	s_mov_b64 s[22:23], s[66:67]
	v_lshl_add_u64 v[26:27], s[4:5], 0, v[18:19]
	v_lshl_add_u64 v[28:29], s[16:17], 0, v[18:19]
	v_lshlrev_b32_e32 v18, 1, v16
	v_lshl_add_u64 v[2:3], s[78:79], 0, v[16:17]
	s_mov_b64 s[4:5], 0x12500000
	v_lshlrev_b64 v[0:1], 11, v[0:1]
	s_ashr_i32 s13, s12, 31
	s_mov_b64 s[14:15], 0x1000
	v_lshl_add_u64 v[30:31], s[90:91], 0, v[18:19]
	v_lshl_add_u64 v[32:33], v[2:3], 0, s[4:5]
	v_mov_b32_e32 v35, v19
	v_lshl_add_u64 v[36:37], s[78:79], 0, v[0:1]
	s_lshl_b64 s[16:17], s[12:13], 11
	v_or_b32_e32 v38, 0x12500400, v16
	v_mov_b32_e32 v39, v19
	v_mov_b32_e32 v18, -1
	s_mov_b64 s[18:19], 0
	s_mov_b64 s[20:21], 0x8500000
	s_mov_b64 s[22:23], 0x8500400
	s_mov_b64 s[24:25], 0x3000
	s_mov_b64 s[26:27], 0x4000
	s_mov_b64 s[28:29], 0x5000
	s_mov_b32 s30, 0x3fb504f3
	s_mov_b32 s34, 0x3d000000
	v_mov_b32_e32 v17, 0x3727c5ac
	s_mov_b32 s13, 0xf800000
	v_mov_b32_e32 v154, 0x260
	s_movk_i32 s35, 0x3fff
	v_readlane_b32 s53, v249, 3
	v_readlane_b32 s54, v249, 4
	v_readlane_b32 s55, v249, 5
	v_readlane_b32 s56, v249, 6
	v_readlane_b32 s57, v249, 7
	v_readlane_b32 s58, v249, 8
	v_readlane_b32 s59, v249, 9
	v_readlane_b32 s60, v249, 10
	v_readlane_b32 s61, v249, 11
	s_branch .LBB0_1595

.LBB0_1603:
	s_cmp_gt_i32 s49, 9
	s_cselect_b64 s[4:5], -1, 0
	s_and_b64 s[0:1], s[6:7], s[4:5]
	s_andn2_b64 vcc, exec, s[0:1]
	s_cbranch_vccnz .LBB0_1753
	s_waitcnt vmcnt(0)
	s_waitcnt vmcnt(0) lgkmcnt(0)
	s_barrier
	s_waitcnt lgkmcnt(0)
	s_mov_b32 s0, s98
	v_mbcnt_lo_u32_b32 v0, -1, 0
	v_mbcnt_hi_u32_b32 v0, -1, v0
	s_nop 1
	v_lshl_add_u32 v0, s0, 6, v0
	s_nop 0
	v_cmp_eq_u32_e32 vcc, 0, v0
	s_and_saveexec_b64 s[6:7], vcc
	s_cbranch_execz .LBB0_1632
	s_add_i32 s0, 0, 0x24800
	v_mov_b32_e32 v0, s0
	s_waitcnt vmcnt(0) expcnt(0) lgkmcnt(0)
	ds_read_b32 v1, v0
	s_add_i32 s0, 0, 0x24804
	v_mov_b32_e32 v0, s0
	ds_read_b32 v0, v0
	s_waitcnt lgkmcnt(1)
	v_cmp_ne_u32_e32 vcc, 0, v1
	s_cbranch_vccz .Lcensus_6

.LBB0_1632:
	s_or_b64 exec, exec, s[6:7]
	s_waitcnt lgkmcnt(0)
	s_mov_b32 s0, s98
	v_mbcnt_lo_u32_b32 v0, -1, 0
	v_mbcnt_hi_u32_b32 v0, -1, v0
	s_nop 1
	v_lshl_add_u32 v6, s0, 6, v0
	s_nop 0
	v_ashrrev_i32_e32 v0, 6, v6
	v_add_u32_e32 v0, -1, v0
	v_cmp_gt_u32_e32 vcc, 3, v0
	s_and_saveexec_b64 s[6:7], vcc
	s_cbranch_execz .LBB0_1722
	s_mul_i32 s0, s33, 6
	s_add_i32 s0, s0, s2
	v_mad_u64_u32 v[2:3], s[0:1], s0, 3, v[0:1]
	s_movk_i32 s0, 0x1d00
	s_nop 0
	v_cmp_gt_i32_e32 vcc, s0, v2
	s_and_b64 exec, exec, vcc
	s_cbranch_execz .LBB0_1722
	s_movk_i32 s1, 0x1100
	s_movk_i32 s0, 0xbff
	v_mov_b32_e32 v1, 0xffffef00
	v_mov_b32_e32 v3, 0xfffff400
	v_cmp_gt_u32_e32 vcc, s1, v2
	v_mov_b32_e32 v4, 0x280
	s_nop 0
	v_cndmask_b32_e32 v1, v1, v3, vcc
	v_cndmask_b32_e64 v3, 2, 1, vcc
	v_cmp_lt_i32_e32 vcc, s0, v2
	s_nop 1
	v_cndmask_b32_e32 v1, v4, v1, vcc
	v_cndmask_b32_e32 v3, 0, v3, vcc
	v_add_u32_e32 v1, v1, v2
	v_cmp_lt_i32_e32 vcc, 0, v3
	s_and_saveexec_b64 s[0:1], vcc
	s_xor_b64 s[0:1], exec, s[0:1]
	s_cbranch_execz .LBB0_1640
	v_cmp_ne_u32_e32 vcc, 1, v3
	s_and_saveexec_b64 s[10:11], vcc
	s_xor_b64 s[10:11], exec, s[10:11]
	s_movk_i32 s3, 0x800
	v_mov_b32_e32 v2, 0x1380
	v_mov_b32_e32 v3, 0xf80
	v_cmp_gt_i32_e32 vcc, s3, v1
	s_nop 1
	v_cndmask_b32_e32 v2, v2, v3, vcc
	v_add_u32_e32 v1, v2, v1
	s_andn2_saveexec_b64 s[10:11], s[10:11]
	v_add_u32_e32 v1, 0x280, v1
	s_or_b64 exec, exec, s[10:11]

.LBB0_1753:
	s_cmp_lt_i32 s48, 10
	s_cselect_b64 s[10:11], -1, 0
	s_and_b64 s[0:1], s[10:11], s[4:5]
	s_andn2_b64 vcc, exec, s[0:1]
	s_cbranch_vccnz .LBB0_1808
	s_cmpk_lt_i32 s2, 0x400
	s_cselect_b64 s[0:1], -1, 0
	s_cmpk_gt_i32 s2, 0x3ff
	s_waitcnt lgkmcnt(0)
	s_mov_b32 s3, s98
	v_mbcnt_lo_u32_b32 v0, -1, 0
	v_mbcnt_hi_u32_b32 v0, -1, v0
	s_nop 1
	v_lshl_add_u32 v0, s3, 6, v0
	s_nop 0
	v_readfirstlane_b32 s18, v0
	s_cbranch_scc1 .LBB0_1756
	s_ashr_i32 s3, s2, 31
	s_lshr_b32 s3, s3, 29
	s_add_i32 s3, s2, s3
	s_ashr_i32 s4, s3, 3
	s_and_b32 s3, s3, -8
	s_sub_i32 s3, s2, s3
	s_lshl_b32 s6, s3, 7
	s_mul_i32 s5, s3, 0x81
	s_cmp_lt_i32 s3, 0
	s_cselect_b32 s3, s5, s6
	s_add_i32 s3, s3, s4
	s_ashr_i32 s4, s3, 31
	s_lshr_b32 s4, s4, 25
	s_add_i32 s4, s3, s4
	s_ashr_i32 s5, s4, 7
	s_and_b32 s4, s4, 0xffffff80
	s_sub_i32 s3, s3, s4
	s_bfe_i32 s4, s3, 0x80000
	s_bfe_u32 s4, s4, 0x3000c
	s_add_i32 s4, s3, s4
	s_bfe_i32 s6, s4, 0x80000
	s_and_b32 s4, s4, 0xf8
	s_sub_i32 s3, s3, s4
	s_lshl_b32 s5, s5, 3
	s_sext_i32_i16 s6, s6
	s_sext_i32_i8 s3, s3
	s_add_i32 s68, s5, s3
	s_ashr_i32 s4, s6, 3

.LBB0_1808:
	s_cmp_gt_i32 s49, 10
	s_cselect_b64 s[4:5], -1, 0
	s_and_b64 s[0:1], s[10:11], s[4:5]
	s_andn2_b64 vcc, exec, s[0:1]
	s_cbranch_vccnz .LBB0_1958
	s_waitcnt vmcnt(0)
	s_waitcnt vmcnt(0) lgkmcnt(0)
	s_barrier
	s_waitcnt lgkmcnt(0)
	s_mov_b32 s0, s98
	v_mbcnt_lo_u32_b32 v0, -1, 0
	v_mbcnt_hi_u32_b32 v0, -1, v0
	s_nop 1
	v_lshl_add_u32 v0, s0, 6, v0
	s_nop 0
	v_cmp_eq_u32_e32 vcc, 0, v0
	s_and_saveexec_b64 s[6:7], vcc
	s_cbranch_execz .LBB0_1837
	s_add_i32 s0, 0, 0x24800
	v_mov_b32_e32 v0, s0
	s_waitcnt vmcnt(0) expcnt(0) lgkmcnt(0)
	ds_read_b32 v1, v0
	s_add_i32 s0, 0, 0x24804
	v_mov_b32_e32 v0, s0
	ds_read_b32 v0, v0
	s_waitcnt lgkmcnt(1)
	v_cmp_ne_u32_e32 vcc, 0, v1
	s_cbranch_vccz .Lcensus_7

.LBB0_1837:
	s_or_b64 exec, exec, s[6:7]
	s_waitcnt lgkmcnt(0)
	s_mov_b32 s0, s98
	v_mbcnt_lo_u32_b32 v0, -1, 0
	v_mbcnt_hi_u32_b32 v0, -1, v0
	s_nop 1
	v_lshl_add_u32 v6, s0, 6, v0
	s_nop 0
	v_ashrrev_i32_e32 v0, 6, v6
	v_add_u32_e32 v0, -1, v0
	v_cmp_gt_u32_e32 vcc, 3, v0
	s_and_saveexec_b64 s[6:7], vcc
	s_cbranch_execz .LBB0_1927
	s_mul_i32 s0, s33, 7
	s_add_i32 s0, s0, s2
	v_mad_u64_u32 v[2:3], s[0:1], s0, 3, v[0:1]
	s_movk_i32 s0, 0x1d00
	s_nop 0
	v_cmp_gt_i32_e32 vcc, s0, v2
	s_and_b64 exec, exec, vcc
	s_cbranch_execz .LBB0_1927
	s_movk_i32 s1, 0x1100
	s_movk_i32 s0, 0xbff
	v_mov_b32_e32 v1, 0xffffef00
	v_mov_b32_e32 v3, 0xfffff400
	v_cmp_gt_u32_e32 vcc, s1, v2
	v_mov_b32_e32 v4, 0x280
	s_nop 0
	v_cndmask_b32_e32 v1, v1, v3, vcc
	v_cndmask_b32_e64 v3, 2, 1, vcc
	v_cmp_lt_i32_e32 vcc, s0, v2
	s_nop 1
	v_cndmask_b32_e32 v1, v4, v1, vcc
	v_cndmask_b32_e32 v3, 0, v3, vcc
	v_add_u32_e32 v1, v1, v2
	v_cmp_lt_i32_e32 vcc, 0, v3
	s_and_saveexec_b64 s[0:1], vcc
	s_xor_b64 s[0:1], exec, s[0:1]
	s_cbranch_execz .LBB0_1845
	v_cmp_ne_u32_e32 vcc, 1, v3
	s_and_saveexec_b64 s[10:11], vcc
	s_xor_b64 s[10:11], exec, s[10:11]
	s_movk_i32 s3, 0x800
	v_mov_b32_e32 v2, 0x1380
	v_mov_b32_e32 v3, 0xf80
	v_cmp_gt_i32_e32 vcc, s3, v1
	s_nop 1
	v_cndmask_b32_e32 v2, v2, v3, vcc
	v_add_u32_e32 v1, v2, v1
	s_andn2_saveexec_b64 s[10:11], s[10:11]
	v_add_u32_e32 v1, 0x280, v1
	s_or_b64 exec, exec, s[10:11]

.LBB0_1958:
	s_cmp_lt_i32 s48, 11
	s_cselect_b64 s[10:11], -1, 0
	s_and_b64 s[0:1], s[10:11], s[4:5]
	s_andn2_b64 vcc, exec, s[0:1]
	s_cbranch_vccnz .LBB0_1973
	s_cmpk_gt_i32 s2, 0x3ff
	s_waitcnt lgkmcnt(0)
	s_mov_b32 s0, s98
	v_mbcnt_lo_u32_b32 v0, -1, 0
	v_mbcnt_hi_u32_b32 v0, -1, v0
	s_nop 1
	v_lshl_add_u32 v158, s0, 6, v0
	s_nop 0
	v_readfirstlane_b32 s30, v158
	s_cbranch_scc1 .LBB0_1972
	s_add_u32 s12, s78, 0x12500000
	s_addc_u32 s13, s79, 0
	s_add_u32 s14, s78, 0x16500000
	s_addc_u32 s15, s79, 0
	s_add_u32 s3, s78, 0x1a500000
	s_addc_u32 s34, s79, 0
	s_lshl_b32 s0, s2, 8
	s_and_b32 s4, s0, 0x700
	s_ashr_i32 s0, s2, 3
	s_ashr_i32 s1, s0, 31
	v_ashrrev_i32_e32 v130, 5, v158
	s_lshl_b64 s[0:1], s[0:1], 7
	v_and_b32_e32 v71, 31, v158
	v_ashrrev_i32_e32 v131, 31, v130
	v_lshlrev_b32_e32 v159, 3, v71
	v_lshl_add_u64 v[0:1], s[0:1], 0, v[130:131]
	v_or_b32_e32 v2, s4, v159
	v_lshlrev_b64 v[14:15], 12, v[0:1]
	v_lshl_or_b32 v14, v2, 1, v14
	s_mov_b64 s[16:17], 0x10000
	v_lshl_add_u64 v[2:3], s[14:15], 0, v[14:15]
	v_lshl_add_u64 v[4:5], v[14:15], 0, s[16:17]
	s_mov_b64 s[18:19], 0x20000
	v_ashrrev_i32_e32 v128, 2, v158
	v_lshl_add_u64 v[6:7], s[14:15], 0, v[4:5]
	global_load_dwordx4 v[16:19], v[2:3], off nt
	global_load_dwordx4 v[20:23], v[6:7], off nt
	v_lshl_add_u64 v[2:3], s[12:13], 0, v[4:5]
	v_lshl_add_u64 v[4:5], v[14:15], 0, s[18:19]
	s_mov_b64 s[20:21], 0x30000
	v_lshl_add_u64 v[6:7], s[14:15], 0, v[4:5]
	v_lshl_add_u64 v[8:9], v[14:15], 0, s[20:21]
	s_mov_b64 s[22:23], 0x40000
	s_mov_b64 s[24:25], 0x50000
	v_ashrrev_i32_e32 v129, 31, v128
	s_add_u32 s6, s78, 0x600000
	v_lshl_add_u64 v[10:11], s[14:15], 0, v[8:9]
	global_load_dwordx4 v[24:27], v[6:7], off nt
	global_load_dwordx4 v[28:31], v[10:11], off nt
	v_lshl_add_u64 v[6:7], s[12:13], 0, v[8:9]
	v_lshl_add_u64 v[8:9], v[14:15], 0, s[22:23]
	v_lshl_add_u64 v[12:13], v[14:15], 0, s[24:25]
	s_waitcnt vmcnt(0)
	v_lshl_add_u64 v[48:49], s[0:1], 0, v[128:129]
	s_addc_u32 s7, s79, 0
	v_and_b32_e32 v64, 3, v158
	v_lshl_add_u64 v[10:11], s[14:15], 0, v[8:9]
	v_lshl_add_u64 v[36:37], s[14:15], 0, v[12:13]
	s_mov_b64 s[26:27], 0x60000
	s_mov_b64 s[28:29], 0x70000
	v_lshlrev_b64 v[48:49], 8, v[48:49]
	v_lshl_add_u64 v[0:1], s[12:13], 0, v[14:15]
	global_load_dwordx4 v[32:35], v[10:11], off nt
	s_nop 0
	global_load_dwordx4 v[36:39], v[36:37], off nt
	v_lshl_add_u64 v[10:11], s[12:13], 0, v[12:13]
	v_lshl_add_u64 v[12:13], v[14:15], 0, s[26:27]
	v_lshl_add_u64 v[14:15], v[14:15], 0, s[28:29]
	v_lshl_add_u64 v[48:49], s[6:7], 0, v[48:49]
	v_lshlrev_b32_e32 v132, 6, v64
	v_mov_b32_e32 v133, 0
	v_lshl_add_u64 v[40:41], s[14:15], 0, v[12:13]
	v_lshl_add_u64 v[44:45], s[14:15], 0, v[14:15]
	v_lshl_add_u64 v[60:61], v[48:49], 0, v[132:133]
	global_load_dwordx4 v[40:43], v[40:41], off nt
	s_nop 0
	global_load_dwordx4 v[44:47], v[44:45], off nt
	s_nop 0
	global_load_dwordx4 v[48:51], v[60:61], off offset:48
	global_load_dwordx4 v[52:55], v[60:61], off offset:32
	global_load_dwordx4 v[56:59], v[60:61], off offset:16
	s_nop 0
	global_load_dwordx4 v[60:63], v[60:61], off
	v_mbcnt_lo_u32_b32 v65, -1, 0
	v_mbcnt_hi_u32_b32 v65, -1, v65
	v_and_b32_e32 v67, 64, v65
	v_xor_b32_e32 v66, 1, v65
	v_add_u32_e32 v67, 64, v67
	v_cmp_lt_i32_e32 vcc, v66, v67
	v_cmp_eq_u32_e64 s[0:1], 0, v64
	v_lshlrev_b32_e32 v64, 4, v158
	v_cndmask_b32_e32 v66, v65, v66, vcc
	v_lshlrev_b32_e32 v160, 2, v66
	v_xor_b32_e32 v66, 2, v65
	v_cmp_lt_i32_e32 vcc, v66, v67
	v_and_b32_e32 v64, 0xf0, v64
	v_lshlrev_b32_e32 v70, 2, v158
	v_cndmask_b32_e32 v65, v65, v66, vcc
	v_lshlrev_b32_e32 v161, 2, v65
	v_mov_b32_e32 v65, v133
	v_lshl_add_u64 v[66:67], s[78:79], 0, v[64:65]
	s_mov_b64 s[36:37], 0x500000
	v_lshl_add_u64 v[136:137], s[6:7], 0, v[132:133]
	s_ashr_i32 s7, s30, 1
	v_bfe_u32 v69, v158, 5, 1
	v_lshl_add_u64 v[134:135], v[66:67], 0, s[36:37]
	v_add_u32_e32 v79, 0, v64
	v_bfe_u32 v64, v158, 2, 2
	s_andn2_b32 s7, s7, 31
	v_and_b32_e32 v65, 16, v158
	v_and_b32_e32 v66, 12, v70
	v_lshl_or_b32 v64, v69, 3, v64
	v_or3_b32 v65, v65, v66, s7
	v_mul_u32_u24_e32 v64, 0x240, v64
	v_lshlrev_b32_e32 v65, 1, v65
	s_add_i32 s31, 0, 0x1ac00
	v_add3_u32 v164, 0, v64, v65
	v_lshlrev_b32_e32 v65, 4, v69
	s_movk_i32 s6, 0x240
	v_add_u32_e32 v81, 0, v65
	v_add_u32_e32 v180, s31, v65
	v_lshl_or_b32 v65, v69, 2, 1
	v_mov_b32_e32 v67, 0x1440
	v_mad_u32_u24 v90, v65, s6, v67
	v_mov_b32_e32 v67, 0x2880
	v_mad_u32_u24 v91, v65, s6, v67
	v_mov_b32_e32 v67, 0x45c0
	v_add_u32_e32 v64, 0x200, v158
	v_mad_u32_u24 v92, v65, s6, v67
	v_mov_b32_e32 v67, 0x5a00
	v_ashrrev_i32_e32 v167, 4, v64
	v_add_u32_e32 v64, 0x400, v158
	v_mad_u32_u24 v93, v65, s6, v67
	v_mov_b32_e32 v67, 0x6e40
	v_ashrrev_i32_e32 v168, 4, v64
	v_add_u32_e32 v64, 0x600, v158
	v_mad_u32_u24 v94, v65, s6, v67
	v_mov_b32_e32 v67, 0x8280
	v_lshl_add_u32 v68, v71, 1, 0
	v_ashrrev_i32_e32 v169, 4, v64
	v_add_u32_e32 v64, 16, v130
	v_mad_u32_u24 v95, v65, s6, v67
	v_mov_b32_e32 v67, 0x9fc0
	v_lshlrev_b32_e32 v78, 3, v128
	v_add_u32_e32 v162, s31, v70
	v_mad_u32_u24 v163, v71, 14, v68
	v_lshl_add_u32 v80, s7, 1, v68
	v_ashrrev_i32_e32 v166, 4, v158
	s_movk_i32 s7, 0x110
	v_mul_lo_u32 v171, v130, s6
	v_add_u32_e32 v66, 32, v130
	v_add_u32_e32 v68, 48, v130
	v_add_u32_e32 v70, 64, v130
	v_add_u32_e32 v72, 0x50, v130
	v_add_u32_e32 v74, 0x60, v130
	v_add_u32_e32 v76, 0x70, v130
	v_mul_u32_u24_e32 v89, 0x240, v65
	v_mad_u32_u24 v96, v65, s6, v67
	v_ashrrev_i32_e32 v65, 31, v64
	s_movk_i32 s4, 0x80
	v_mul_lo_u32 v82, v166, s7
	v_mul_lo_u32 v83, v167, s7
	v_mul_lo_u32 v84, v168, s7
	v_mul_lo_u32 v85, v169, s7
	v_lshlrev_b32_e32 v172, 3, v64
	v_add_u32_e32 v86, 0x9000, v171
	v_mul_u32_u24_e32 v87, 0x110, v71
	v_mul_u32_u24_e32 v88, 0x900, v69
	v_lshlrev_b64 v[140:141], 11, v[64:65]
	v_ashrrev_i32_e32 v67, 31, v66
	v_ashrrev_i32_e32 v69, 31, v68
	v_ashrrev_i32_e32 v71, 31, v70
	v_ashrrev_i32_e32 v73, 31, v72
	v_ashrrev_i32_e32 v75, 31, v74
	v_ashrrev_i32_e32 v77, 31, v76
	s_add_i32 s6, s2, s33
	v_add_u32_e32 v64, 0, v78
	v_lshl_add_u64 v[4:5], s[12:13], 0, v[4:5]
	v_lshl_add_u64 v[8:9], s[12:13], 0, v[8:9]
	v_lshl_add_u64 v[12:13], s[12:13], 0, v[12:13]
	v_lshl_add_u64 v[14:15], s[12:13], 0, v[14:15]
	s_mov_b32 s35, -1
	v_cmp_gt_i32_e64 s[4:5], s4, v158
	v_add_u32_e32 v165, 0x8800, v164
	v_lshlrev_b32_e32 v170, 3, v130
	v_lshlrev_b32_e32 v173, 3, v66
	v_lshlrev_b32_e32 v174, 3, v68
	v_lshlrev_b32_e32 v175, 3, v70
	v_lshlrev_b32_e32 v176, 3, v72
	v_lshlrev_b32_e32 v177, 3, v74
	v_lshlrev_b32_e32 v178, 3, v76
	v_add_u32_e32 v179, 0x18d00, v164
	v_add_u32_e32 v181, 32, v180
	v_add_u32_e32 v182, 64, v180
	v_add_u32_e32 v183, 0x60, v180
	v_add_u32_e32 v184, 0x80, v180
	v_add_u32_e32 v185, 0xa0, v180
	v_add_u32_e32 v186, 0xc0, v180
	v_add_u32_e32 v187, 0xe0, v180
	v_add_u32_e32 v188, 0x100, v180
	v_add_u32_e32 v189, 0x120, v180
	v_add_u32_e32 v190, 0x140, v180
	v_add_u32_e32 v191, 0x160, v180
	v_add_u32_e32 v192, 0x180, v180
	v_add_u32_e32 v193, 0x1a0, v180
	v_add_u32_e32 v194, 0x1c0, v180
	v_add_u32_e32 v195, 0x1e0, v180
	v_lshlrev_b64 v[138:139], 11, v[130:131]
	v_lshlrev_b64 v[142:143], 11, v[66:67]
	v_lshlrev_b64 v[144:145], 11, v[68:69]
	v_lshlrev_b64 v[146:147], 11, v[70:71]
	v_lshlrev_b64 v[148:149], 11, v[72:73]
	v_lshlrev_b64 v[150:151], 11, v[74:75]
	v_lshlrev_b64 v[152:153], 11, v[76:77]
	s_lshl_b32 s36, s6, 8
	s_lshl_b32 s37, s33, 8
	s_mov_b32 s38, 0x3a000000
	v_add_u32_e32 v196, 0x1a800, v64
	s_mov_b32 s39, 0xf800000
	v_mov_b32_e32 v197, 0x260
	v_add_u32_e32 v198, v79, v82
	v_add_u32_e32 v199, v79, v83
	v_add_u32_e32 v200, v79, v84
	v_add_u32_e32 v201, v79, v85
	v_add_u32_e32 v202, v81, v87
	v_add_u32_e32 v203, v80, v88
	v_add_u32_e32 v204, v80, v89
	v_add_u32_e32 v205, v80, v90
	v_add_u32_e32 v206, v80, v91
	v_add_u32_e32 v207, v80, v92
	v_add_u32_e32 v208, v80, v93
	v_add_u32_e32 v209, v80, v94
	v_add_u32_e32 v210, v80, v95
	v_add_u32_e32 v211, v80, v96
	s_mov_b32 s40, 0xc3e00000
	v_add_u32_e32 v212, v163, v86
	v_mov_b32_e32 v213, 0x43e00000
	s_mov_b32 s42, s2
	s_branch .LBB0_1962

.LBB0_1973:
	s_cmp_gt_i32 s49, 11
	s_cselect_b64 s[6:7], -1, 0
	s_and_b64 s[0:1], s[10:11], s[6:7]
	s_andn2_b64 vcc, exec, s[0:1]
	s_cbranch_vccnz .LBB0_2123
	s_waitcnt vmcnt(0)
	s_waitcnt vmcnt(0) lgkmcnt(0)
	s_barrier
	s_waitcnt lgkmcnt(0)
	s_mov_b32 s0, s98
	v_mbcnt_lo_u32_b32 v0, -1, 0
	v_mbcnt_hi_u32_b32 v0, -1, v0
	s_nop 1
	v_lshl_add_u32 v0, s0, 6, v0
	s_nop 0
	v_cmp_eq_u32_e32 vcc, 0, v0
	s_and_saveexec_b64 s[4:5], vcc
	s_cbranch_execz .LBB0_2002
	s_add_i32 s0, 0, 0x24800
	v_mov_b32_e32 v0, s0
	s_waitcnt vmcnt(0) expcnt(0) lgkmcnt(0)
	ds_read_b32 v1, v0
	s_add_i32 s0, 0, 0x24804
	v_mov_b32_e32 v0, s0
	ds_read_b32 v0, v0
	s_waitcnt lgkmcnt(1)
	v_cmp_ne_u32_e32 vcc, 0, v1
	s_cbranch_vccz .Lcensus_8

.LBB0_2002:
	s_or_b64 exec, exec, s[4:5]
	s_waitcnt lgkmcnt(0)
	s_mov_b32 s0, s98
	v_mbcnt_lo_u32_b32 v0, -1, 0
	v_mbcnt_hi_u32_b32 v0, -1, v0
	s_nop 1
	v_lshl_add_u32 v6, s0, 6, v0
	s_nop 0
	v_ashrrev_i32_e32 v0, 6, v6
	v_add_u32_e32 v0, -1, v0
	v_cmp_gt_u32_e32 vcc, 3, v0
	s_and_saveexec_b64 s[4:5], vcc
	s_cbranch_execz .LBB0_2092
	s_lshl_b32 s0, s33, 3
	s_add_i32 s0, s0, s2
	v_mad_u64_u32 v[2:3], s[0:1], s0, 3, v[0:1]
	s_movk_i32 s0, 0x1d00
	s_nop 0
	v_cmp_gt_i32_e32 vcc, s0, v2
	s_and_b64 exec, exec, vcc
	s_cbranch_execz .LBB0_2092
	s_movk_i32 s1, 0x1100
	s_movk_i32 s0, 0xbff
	v_mov_b32_e32 v1, 0xffffef00
	v_mov_b32_e32 v3, 0xfffff400
	v_cmp_gt_u32_e32 vcc, s1, v2
	v_mov_b32_e32 v4, 0x280
	s_nop 0
	v_cndmask_b32_e32 v1, v1, v3, vcc
	v_cndmask_b32_e64 v3, 2, 1, vcc
	v_cmp_lt_i32_e32 vcc, s0, v2
	s_nop 1
	v_cndmask_b32_e32 v1, v4, v1, vcc
	v_cndmask_b32_e32 v3, 0, v3, vcc
	v_add_u32_e32 v1, v1, v2
	v_cmp_lt_i32_e32 vcc, 0, v3
	s_and_saveexec_b64 s[0:1], vcc
	s_xor_b64 s[0:1], exec, s[0:1]
	s_cbranch_execz .LBB0_2010
	v_cmp_ne_u32_e32 vcc, 1, v3
	s_and_saveexec_b64 s[10:11], vcc
	s_xor_b64 s[10:11], exec, s[10:11]
	s_movk_i32 s3, 0x800
	v_mov_b32_e32 v2, 0x1380
	v_mov_b32_e32 v3, 0xf80
	v_cmp_gt_i32_e32 vcc, s3, v1
	s_nop 1
	v_cndmask_b32_e32 v2, v2, v3, vcc
	v_add_u32_e32 v1, v2, v1
	s_andn2_saveexec_b64 s[10:11], s[10:11]
	v_add_u32_e32 v1, 0x280, v1
	s_or_b64 exec, exec, s[10:11]

.LBB0_2123:
	s_cmp_lt_i32 s48, 12
	s_cselect_b64 s[10:11], -1, 0
	s_cmp_gt_i32 s48, 11
	s_cselect_b64 s[4:5], -1, 0
	s_and_b64 s[0:1], s[10:11], s[6:7]
	s_andn2_b64 vcc, exec, s[0:1]
	s_cbranch_vccnz .LBB0_2144
	s_cmpk_gt_i32 s2, 0xff
	s_waitcnt lgkmcnt(0)
	s_mov_b32 s0, s98
	v_mbcnt_lo_u32_b32 v0, -1, 0
	v_mbcnt_hi_u32_b32 v0, -1, v0
	s_nop 1
	v_lshl_add_u32 v0, s0, 6, v0
	s_nop 0
	v_readfirstlane_b32 s1, v0
	s_cbranch_scc1 .LBB0_2144
	v_bfe_i32 v3, v0, 27, 1
	v_lshlrev_b32_e32 v1, 4, v0
	v_lshrrev_b32_e32 v3, 22, v3
	v_add_u32_e32 v3, v1, v3
	v_and_b32_e32 v3, 0xfffffc00, v3
	v_ashrrev_i32_e32 v2, 31, v0
	v_sub_u32_e32 v1, v1, v3
	v_lshrrev_b32_e32 v2, 26, v2
	v_lshrrev_b32_e32 v3, 4, v1
	v_add_u32_e32 v2, v0, v2
	v_bitop3_b32 v3, v3, v1, 32 bitop3:0x6c
	v_ashrrev_i32_e32 v1, 31, v1
	s_add_u32 s3, s78, 0x1a500000
	v_ashrrev_i32_e32 v2, 6, v2
	v_lshrrev_b32_e32 v1, 26, v1
	s_addc_u32 s15, s79, 0
	v_lshlrev_b32_e32 v4, 3, v2
	v_add_u32_e32 v1, v3, v1
	s_add_u32 s17, s78, 0x2100000
	v_and_b32_e32 v4, -16, v4
	v_ashrrev_i32_e32 v1, 6, v1
	s_addc_u32 s38, s79, 0
	v_add_u32_e32 v4, v1, v4
	v_mul_i32_i24_e32 v5, 64, v1
	v_and_b32_e32 v1, 3, v1
	s_mov_b32 s0, 0x1fffe0
	s_ashr_i32 s40, s2, 31
	v_and_or_b32 v1, v4, s0, v1
	s_lshr_b32 s0, s40, 29
	s_add_i32 s0, s2, s0
	s_ashr_i32 s6, s0, 3
	s_and_b32 s0, s0, -8
	s_ashr_i32 s12, s1, 6
	s_sub_i32 s0, s2, s0
	s_ashr_i32 s13, s1, 8
	s_lshl_b32 s39, s12, 10
	s_lshl_b32 s14, s0, 5
	s_mul_i32 s7, s0, 33
	s_cmp_lt_i32 s0, 0
	s_cselect_b32 s0, s7, s14
	s_add_i32 s0, s0, s6
	s_ashr_i32 s6, s0, 31
	s_lshr_b32 s6, s6, 27
	s_add_i32 s6, s0, s6
	s_ashr_i32 s7, s6, 5
	s_and_b32 s6, s6, 0xffe0
	s_sub_i32 s6, s0, s6
	s_bfe_i32 s0, s6, 0x80000
	s_bfe_u32 s0, s0, 0x3000c
	s_add_i32 s14, s6, s0
	s_bfe_i32 s0, s14, 0x80000
	s_and_b32 s14, s14, 0xf8
	s_sub_i32 s6, s6, s14
	s_lshl_b32 s7, s7, 3
	s_sext_i32_i8 s6, s6
	s_add_i32 s26, s7, s6
	s_sext_i32_i16 s0, s0
	s_ashr_i32 s27, s26, 31
	s_lshr_b32 s0, s0, 3
	s_lshl_b64 s[6:7], s[26:27], 19
	v_sub_u32_e32 v3, v3, v5
	v_mov_b32_e32 v5, 1
	s_add_u32 s28, s3, s6
	v_lshlrev_b32_e32 v2, 5, v2
	v_ashrrev_i16_sdwa v3, v5, sext(v3) dst_sel:DWORD dst_unused:UNUSED_PAD src0_sel:DWORD src1_sel:BYTE_0
	v_lshlrev_b32_e32 v5, 1, v4
	v_lshrrev_b32_e32 v6, 2, v4
	s_addc_u32 s29, s15, s7
	s_bfe_i64 s[6:7], s[0:1], 0x100000
	v_and_b32_e32 v2, 32, v2
	v_bfe_i32 v3, v3, 0, 16
	v_and_b32_e32 v5, 24, v5
	v_and_b32_e32 v6, 4, v6
	s_lshl_b64 s[6:7], s[6:7], 19
	v_or3_b32 v1, v1, v6, v5
	v_add_lshl_u32 v2, v2, v3, 1
	s_add_u32 s30, s17, s6
	v_lshl_add_u32 v174, v1, 11, v2
	s_addc_u32 s31, s38, s7
	s_add_i32 s27, s39, 0
	s_mov_b64 s[6:7], s[30:31]
	s_add_i32 m0, s27, 0x10000
	v_lshl_add_u32 v175, v4, 11, v2
	global_load_lds_dwordx4 v174, s[6:7]
	s_add_u32 s6, s30, 0x20000
	s_addc_u32 s7, s31, 0
	s_add_i32 m0, s27, 0x12000
	s_nop 0
	global_load_lds_dwordx4 v174, s[6:7]
	s_add_i32 m0, s27, 0x14000
	s_add_u32 s6, s30, 0x40000
	s_addc_u32 s7, s31, 0
	s_nop 0
	global_load_lds_dwordx4 v174, s[6:7]
	s_add_u32 s6, s30, 0x60000
	s_addc_u32 s7, s31, 0
	s_add_i32 m0, s27, 0x16000
	s_nop 0
	global_load_lds_dwordx4 v174, s[6:7]
	s_mov_b64 s[6:7], s[28:29]
	s_mov_b32 m0, s27
	s_nop 0
	global_load_lds_dwordx4 v175, s[6:7]
	s_add_u32 s6, s28, 0x20000
	s_addc_u32 s7, s29, 0
	s_add_i32 s41, s27, 0x2000
	s_mov_b32 m0, s41
	s_add_i32 s42, s27, 0x4000
	global_load_lds_dwordx4 v175, s[6:7]
	s_add_u32 s6, s28, 0x40000
	s_addc_u32 s7, s29, 0
	s_mov_b32 m0, s42
	s_nop 0
	global_load_lds_dwordx4 v175, s[6:7]
	s_add_u32 s6, s28, 0x60000
	s_addc_u32 s7, s29, 0
	s_add_i32 s43, s27, 0x6000
	s_mov_b32 m0, s43
	s_cmp_eq_u32 s13, 1
	global_load_lds_dwordx4 v175, s[6:7]
	s_cselect_b64 s[6:7], -1, 0
	s_cmp_lg_u32 s13, 1
	s_cbranch_scc1 .LBB0_2127
	s_barrier

.LBB0_2144:
	s_cmp_gt_i32 s49, 12
	s_cselect_b64 s[12:13], -1, 0
	s_and_b64 s[0:1], s[10:11], s[12:13]
	s_andn2_b64 vcc, exec, s[0:1]
	s_cbranch_vccnz .LBB0_2302
	s_waitcnt vmcnt(0)
	s_waitcnt vmcnt(0) lgkmcnt(0)
	s_barrier
	s_waitcnt lgkmcnt(0)
	s_mov_b32 s0, s98
	v_mbcnt_lo_u32_b32 v0, -1, 0
	v_mbcnt_hi_u32_b32 v0, -1, v0
	s_nop 1
	v_lshl_add_u32 v0, s0, 6, v0
	s_nop 0
	v_cmp_eq_u32_e32 vcc, 0, v0
	s_and_saveexec_b64 s[6:7], vcc
	s_cbranch_execz .LBB0_2173
	s_add_i32 s0, 0, 0x24800
	v_mov_b32_e32 v0, s0
	s_waitcnt vmcnt(0) expcnt(0) lgkmcnt(0)
	ds_read_b32 v1, v0
	s_add_i32 s0, 0, 0x24804
	v_mov_b32_e32 v0, s0
	ds_read_b32 v0, v0
	s_waitcnt lgkmcnt(1)
	v_cmp_ne_u32_e32 vcc, 0, v1
	s_cbranch_vccz .Lcensus_9

.LBB0_2173:
	s_or_b64 exec, exec, s[6:7]
	v_mbcnt_lo_u32_b32 v1, -1, 0
	v_mbcnt_hi_u32_b32 v1, -1, v1
	v_mov_b32_e32 v44, 0
	v_mov_b32_e32 v45, 0
	v_mov_b32_e32 v46, 0
	s_waitcnt lgkmcnt(0)
	s_mov_b32 s0, s98
	v_mov_b32_e32 v47, 0
	v_mov_b32_e32 v38, 0
	v_lshl_add_u32 v52, s0, 6, v1
	s_movk_i32 s0, 0x100
	v_ashrrev_i32_e32 v53, 31, v52
	v_lshl_add_u64 v[32:33], v[52:53], 4, s[78:79]
	v_add_co_u32_e32 v8, vcc, 0x1212000, v32
	v_cmp_gt_i32_e64 s[0:1], s0, v52
	s_nop 0
	v_addc_co_u32_e32 v9, vcc, 0, v33, vcc
	v_add_co_u32_e32 v10, vcc, 0x1214000, v32
	v_mov_b32_e32 v39, 0
	s_nop 0
	v_addc_co_u32_e32 v11, vcc, 0, v33, vcc
	v_add_co_u32_e32 v16, vcc, 0x1216000, v32
	global_load_dwordx4 v[0:3], v[8:9], off
	global_load_dwordx4 v[4:7], v[10:11], off
	v_addc_co_u32_e32 v17, vcc, 0, v33, vcc
	v_add_co_u32_e32 v18, vcc, 0x1218000, v32
	v_mov_b32_e32 v58, 0
	s_nop 0
	v_addc_co_u32_e32 v19, vcc, 0, v33, vcc
	v_add_co_u32_e32 v24, vcc, 0x121a000, v32
	global_load_dwordx4 v[8:11], v[16:17], off
	global_load_dwordx4 v[12:15], v[18:19], off
	v_addc_co_u32_e32 v25, vcc, 0, v33, vcc
	v_add_co_u32_e32 v26, vcc, 0x121c000, v32
	v_mov_b32_e32 v59, 0
	s_nop 0
	v_addc_co_u32_e32 v27, vcc, 0, v33, vcc
	v_add_co_u32_e32 v34, vcc, 0x121e000, v32
	global_load_dwordx4 v[16:19], v[24:25], off
	global_load_dwordx4 v[20:23], v[26:27], off
	v_addc_co_u32_e32 v35, vcc, 0, v33, vcc
	v_add_co_u32_e32 v36, vcc, 0x1220000, v32
	v_mov_b32_e32 v60, 0
	s_nop 0
	v_addc_co_u32_e32 v37, vcc, 0, v33, vcc
	v_add_co_u32_e32 v32, vcc, 0x1222000, v32
	global_load_dwordx4 v[24:27], v[34:35], off
	global_load_dwordx4 v[28:31], v[36:37], off
	v_addc_co_u32_e32 v33, vcc, 0, v33, vcc
	global_load_dwordx4 v[40:43], v[32:33], off
	v_mov_b32_e32 v32, 0
	v_mov_b32_e32 v33, 0
	v_mov_b32_e32 v34, 0
	v_mov_b32_e32 v35, 0
	v_mov_b32_e32 v36, 0
	v_mov_b32_e32 v37, 0
	v_mov_b32_e32 v61, 0
	v_mov_b32_e32 v54, 0
	v_mov_b32_e32 v55, 0
	v_mov_b32_e32 v56, 0
	v_mov_b32_e32 v57, 0
	v_mov_b32_e32 v48, 0
	v_mov_b32_e32 v49, 0
	v_mov_b32_e32 v50, 0
	v_mov_b32_e32 v51, 0
	s_and_saveexec_b64 s[6:7], s[0:1]
	s_cbranch_execz .LBB0_2175
	v_lshlrev_b32_e32 v32, 2, v52
	v_readlane_b32 s16, v249, 2
	v_ashrrev_i32_e32 v33, 31, v32
	v_readlane_b32 s26, v249, 12
	v_readlane_b32 s27, v249, 13
	v_lshlrev_b64 v[44:45], 2, v[32:33]
	s_mov_b64 s[14:15], s[26:27]
	v_readlane_b32 s17, v249, 3
	v_readlane_b32 s18, v249, 4
	v_readlane_b32 s19, v249, 5
	v_readlane_b32 s28, v249, 14
	v_readlane_b32 s29, v249, 15
	v_lshl_add_u64 v[32:33], s[14:15], 0, v[44:45]
	v_readlane_b32 s30, v249, 16
	v_readlane_b32 s31, v249, 17
	s_mov_b64 s[16:17], s[28:29]
	v_add_co_u32_e32 v32, vcc, 0x2000, v32
	v_lshl_add_u64 v[36:37], s[16:17], 0, v[44:45]
	s_nop 0
	v_addc_co_u32_e32 v33, vcc, 0, v33, vcc
	v_add_co_u32_e32 v36, vcc, 0x2000, v36
	v_lshl_add_u64 v[44:45], s[78:79], 0, v[44:45]
	s_nop 0
	v_addc_co_u32_e32 v37, vcc, 0, v37, vcc
	v_add_co_u32_e32 v46, vcc, 0x50000, v44
	global_load_dwordx4 v[32:35], v[32:33], off
	s_nop 0
	v_addc_co_u32_e32 v47, vcc, 0, v45, vcc
	v_add_co_u32_e32 v48, vcc, 0x4f000, v44
	global_load_dwordx4 v[36:39], v[36:37], off
	s_nop 0
	v_addc_co_u32_e32 v49, vcc, 0, v45, vcc
	global_load_dwordx4 v[54:57], v[46:47], off
	s_nop 0
	global_load_dwordx4 v[48:51], v[48:49], off
	v_add_co_u32_e32 v46, vcc, 0x56000, v44
	v_readlane_b32 s20, v249, 6
	s_nop 0
	v_addc_co_u32_e32 v47, vcc, 0, v45, vcc
	v_add_co_u32_e32 v44, vcc, 0x55000, v44
	global_load_dwordx4 v[62:65], v[46:47], off
	s_nop 0
	v_addc_co_u32_e32 v45, vcc, 0, v45, vcc
	global_load_dwordx4 v[44:47], v[44:45], off
	v_readlane_b32 s21, v249, 7
	v_readlane_b32 s22, v249, 8
	v_readlane_b32 s23, v249, 9
	v_readlane_b32 s24, v249, 10
	v_readlane_b32 s25, v249, 11
	s_mov_b64 s[18:19], s[30:31]
	s_waitcnt vmcnt(3)
	v_pk_add_f32 v[60:61], v[56:57], 1.0 op_sel_hi:[1,0]
	v_pk_add_f32 v[58:59], v[54:55], 1.0 op_sel_hi:[1,0]
	s_waitcnt vmcnt(1)
	v_pk_add_f32 v[56:57], v[64:65], 1.0 op_sel_hi:[1,0]
	v_pk_add_f32 v[54:55], v[62:63], 1.0 op_sel_hi:[1,0]

.LBB0_2179:
	s_or_b64 exec, exec, s[6:7]
	s_waitcnt lgkmcnt(0)
	s_barrier
	s_waitcnt lgkmcnt(0)
	s_mov_b32 s0, s98
	v_mbcnt_lo_u32_b32 v0, -1, 0
	v_mbcnt_hi_u32_b32 v0, -1, v0
	s_nop 1
	v_lshl_add_u32 v6, s0, 6, v0
	s_nop 0
	v_ashrrev_i32_e32 v0, 6, v6
	v_add_u32_e32 v0, -1, v0
	v_cmp_gt_u32_e32 vcc, 3, v0
	s_and_saveexec_b64 s[6:7], vcc
	s_cbranch_execz .LBB0_2269
	s_mul_i32 s0, s33, 9
	s_add_i32 s0, s0, s2
	v_mad_u64_u32 v[2:3], s[0:1], s0, 3, v[0:1]
	s_movk_i32 s0, 0x1d00
	s_nop 0
	v_cmp_gt_i32_e32 vcc, s0, v2
	s_and_b64 exec, exec, vcc
	s_cbranch_execz .LBB0_2269
	s_movk_i32 s1, 0x1100
	s_movk_i32 s0, 0xbff
	v_mov_b32_e32 v1, 0xffffef00
	v_mov_b32_e32 v3, 0xfffff400
	v_cmp_gt_u32_e32 vcc, s1, v2
	v_mov_b32_e32 v4, 0x280
	s_nop 0
	v_cndmask_b32_e32 v1, v1, v3, vcc
	v_cndmask_b32_e64 v3, 2, 1, vcc
	v_cmp_lt_i32_e32 vcc, s0, v2
	s_nop 1
	v_cndmask_b32_e32 v1, v4, v1, vcc
	v_cndmask_b32_e32 v3, 0, v3, vcc
	v_add_u32_e32 v1, v1, v2
	v_cmp_lt_i32_e32 vcc, 0, v3
	s_and_saveexec_b64 s[0:1], vcc
	s_xor_b64 s[0:1], exec, s[0:1]
	s_cbranch_execz .LBB0_2187
	v_cmp_ne_u32_e32 vcc, 1, v3
	s_and_saveexec_b64 s[10:11], vcc
	s_xor_b64 s[10:11], exec, s[10:11]
	s_movk_i32 s3, 0x800
	v_mov_b32_e32 v2, 0x1380
	v_mov_b32_e32 v3, 0xf80
	v_cmp_gt_i32_e32 vcc, s3, v1
	s_nop 1
	v_cndmask_b32_e32 v2, v2, v3, vcc
	v_add_u32_e32 v1, v2, v1
	s_andn2_saveexec_b64 s[10:11], s[10:11]
	v_add_u32_e32 v1, 0x280, v1
	s_or_b64 exec, exec, s[10:11]

.LBB0_2302:
	s_add_u32 s6, s78, 0xc00000
	s_addc_u32 s7, s79, 0
	s_add_u32 s10, s78, 0x1000000
	s_addc_u32 s11, s79, 0
	s_cmp_lt_i32 s48, 13
	s_cselect_b64 s[14:15], -1, 0
	s_and_b64 s[0:1], s[14:15], s[12:13]
	s_andn2_b64 vcc, exec, s[0:1]
	s_cbranch_vccnz .LBB0_2335
	v_mbcnt_lo_u32_b32 v1, -1, 0
	v_mbcnt_hi_u32_b32 v1, -1, v1
	s_lshl_b32 s0, s2, 5
	v_mov_b32_e32 v87, 0
	s_andn2_b64 vcc, exec, s[4:5]
	s_waitcnt lgkmcnt(0)
	s_mov_b32 s1, s98
	s_nop 1
	v_lshl_add_u32 v114, s1, 6, v1
	s_nop 0
	v_ashrrev_i32_e32 v97, 6, v114
	v_bfe_u32 v115, v114, 4, 2
	v_and_b32_e32 v98, 15, v114
	v_lshl_add_u32 v96, v97, 2, s0
	v_or_b32_e32 v0, v96, v115
	v_lshlrev_b32_e32 v116, 3, v98
	v_lshl_or_b32 v86, v0, 10, v116
	v_lshl_add_u64 v[0:1], v[86:87], 1, s[76:77]
	global_load_dwordx4 v[60:63], v[0:1], off nt
	global_load_dwordx4 v[56:59], v[0:1], off offset:256 nt
	global_load_dwordx4 v[52:55], v[0:1], off offset:512 nt
	global_load_dwordx4 v[48:51], v[0:1], off offset:768 nt
	global_load_dwordx4 v[44:47], v[0:1], off offset:1024 nt
	global_load_dwordx4 v[40:43], v[0:1], off offset:1280 nt
	global_load_dwordx4 v[36:39], v[0:1], off offset:1536 nt
	global_load_dwordx4 v[32:35], v[0:1], off offset:1792 nt
	s_cbranch_vccnz .LBB0_2311
	v_mbcnt_lo_u32_b32 v1, -1, 0
	v_mbcnt_hi_u32_b32 v1, -1, v1
	v_mov_b32_e32 v77, 0
	v_mov_b32_e32 v78, 0
	v_mov_b32_e32 v79, 0
	s_waitcnt lgkmcnt(0)
	s_mov_b32 s0, s98
	v_mov_b32_e32 v70, 0
	v_mov_b32_e32 v71, 0
	v_lshl_add_u32 v84, s0, 6, v1
	s_movk_i32 s0, 0x100
	v_ashrrev_i32_e32 v85, 31, v84
	v_lshl_add_u64 v[28:29], v[84:85], 4, s[78:79]
	v_add_co_u32_e32 v8, vcc, 0x1212000, v28
	v_cmp_gt_i32_e64 s[0:1], s0, v84
	s_nop 0
	v_addc_co_u32_e32 v9, vcc, 0, v29, vcc
	v_add_co_u32_e32 v10, vcc, 0x1214000, v28
	v_mov_b32_e32 v92, 0
	s_nop 0
	v_addc_co_u32_e32 v11, vcc, 0, v29, vcc
	v_add_co_u32_e32 v16, vcc, 0x1216000, v28
	global_load_dwordx4 v[0:3], v[8:9], off
	global_load_dwordx4 v[4:7], v[10:11], off
	v_addc_co_u32_e32 v17, vcc, 0, v29, vcc
	v_add_co_u32_e32 v18, vcc, 0x1218000, v28
	v_mov_b32_e32 v93, 0
	s_nop 0
	v_addc_co_u32_e32 v19, vcc, 0, v29, vcc
	v_add_co_u32_e32 v24, vcc, 0x121a000, v28
	global_load_dwordx4 v[8:11], v[16:17], off
	global_load_dwordx4 v[12:15], v[18:19], off
	v_addc_co_u32_e32 v25, vcc, 0, v29, vcc
	v_add_co_u32_e32 v26, vcc, 0x121c000, v28
	v_mov_b32_e32 v94, 0
	s_nop 0
	v_addc_co_u32_e32 v27, vcc, 0, v29, vcc
	v_add_co_u32_e32 v30, vcc, 0x121e000, v28
	global_load_dwordx4 v[16:19], v[24:25], off
	global_load_dwordx4 v[20:23], v[26:27], off
	v_addc_co_u32_e32 v31, vcc, 0, v29, vcc
	v_add_co_u32_e32 v68, vcc, 0x1220000, v28
	v_mov_b32_e32 v95, 0
	s_nop 0
	v_addc_co_u32_e32 v69, vcc, 0, v29, vcc
	v_add_co_u32_e32 v28, vcc, 0x1222000, v28
	global_load_dwordx4 v[24:27], v[30:31], off
	global_load_dwordx4 v[64:67], v[68:69], off
	v_addc_co_u32_e32 v29, vcc, 0, v29, vcc
	global_load_dwordx4 v[72:75], v[28:29], off
	v_mov_b32_e32 v28, 0
	v_mov_b32_e32 v29, 0
	v_mov_b32_e32 v30, 0
	v_mov_b32_e32 v31, 0
	v_mov_b32_e32 v68, 0
	v_mov_b32_e32 v69, 0
	v_mov_b32_e32 v88, 0
	v_mov_b32_e32 v89, 0
	v_mov_b32_e32 v90, 0
	v_mov_b32_e32 v91, 0
	v_mov_b32_e32 v80, 0
	v_mov_b32_e32 v81, 0
	v_mov_b32_e32 v82, 0
	v_mov_b32_e32 v83, 0
	s_and_saveexec_b64 s[4:5], s[0:1]
	s_cbranch_execz .LBB0_2306
	v_lshlrev_b32_e32 v28, 2, v84
	v_readlane_b32 s16, v249, 2
	v_ashrrev_i32_e32 v29, 31, v28
	v_readlane_b32 s18, v249, 4
	v_readlane_b32 s19, v249, 5
	v_readlane_b32 s26, v249, 12
	v_readlane_b32 s27, v249, 13
	v_lshlrev_b64 v[76:77], 2, v[28:29]
	s_mov_b64 s[18:19], s[26:27]
	v_readlane_b32 s20, v249, 6
	v_readlane_b32 s21, v249, 7
	v_readlane_b32 s28, v249, 14
	v_readlane_b32 s29, v249, 15
	v_lshl_add_u64 v[28:29], s[18:19], 0, v[76:77]
	s_mov_b64 s[20:21], s[28:29]
	v_add_co_u32_e32 v28, vcc, 0x2000, v28
	v_lshl_add_u64 v[68:69], s[20:21], 0, v[76:77]
	s_nop 0
	v_addc_co_u32_e32 v29, vcc, 0, v29, vcc
	v_add_co_u32_e32 v68, vcc, 0x2000, v68
	v_lshl_add_u64 v[76:77], s[78:79], 0, v[76:77]
	s_nop 0
	v_addc_co_u32_e32 v69, vcc, 0, v69, vcc
	v_add_co_u32_e32 v78, vcc, 0x50000, v76
	global_load_dwordx4 v[28:31], v[28:29], off
	s_nop 0
	v_addc_co_u32_e32 v79, vcc, 0, v77, vcc
	v_add_co_u32_e32 v90, vcc, 0x4f000, v76
	global_load_dwordx4 v[86:89], v[78:79], off
	s_nop 0
	v_addc_co_u32_e32 v91, vcc, 0, v77, vcc
	v_add_co_u32_e32 v78, vcc, 0x56000, v76
	global_load_dwordx4 v[68:71], v[68:69], off
	s_nop 0
	v_addc_co_u32_e32 v79, vcc, 0, v77, vcc
	v_add_co_u32_e32 v92, vcc, 0x55000, v76
	global_load_dwordx4 v[100:103], v[78:79], off
	s_nop 0
	v_addc_co_u32_e32 v93, vcc, 0, v77, vcc
	global_load_dwordx4 v[76:79], v[92:93], off
	global_load_dwordx4 v[80:83], v[90:91], off
	v_readlane_b32 s17, v249, 3
	v_readlane_b32 s22, v249, 8
	v_readlane_b32 s23, v249, 9
	v_readlane_b32 s24, v249, 10
	v_readlane_b32 s25, v249, 11
	v_readlane_b32 s30, v249, 16
	v_readlane_b32 s31, v249, 17
	s_waitcnt vmcnt(0)
	v_pk_add_f32 v[94:95], v[88:89], 1.0 op_sel_hi:[1,0]
	v_pk_add_f32 v[92:93], v[86:87], 1.0 op_sel_hi:[1,0]
	v_pk_add_f32 v[90:91], v[102:103], 1.0 op_sel_hi:[1,0]
	v_pk_add_f32 v[88:89], v[100:101], 1.0 op_sel_hi:[1,0]
	v_mov_b32_e32 v87, v76

.LBB0_2335:
	s_cmp_gt_i32 s49, 13
	s_cselect_b64 s[4:5], -1, 0
	s_and_b64 s[0:1], s[14:15], s[4:5]
	s_andn2_b64 vcc, exec, s[0:1]
	s_cbranch_vccnz .LBB0_2397
	s_waitcnt vmcnt(0)
	s_waitcnt vmcnt(0) lgkmcnt(0)
	s_barrier
	s_waitcnt lgkmcnt(0)
	s_mov_b32 s0, s98
	v_mbcnt_lo_u32_b32 v0, -1, 0
	v_mbcnt_hi_u32_b32 v0, -1, v0
	s_nop 1
	v_lshl_add_u32 v0, s0, 6, v0
	s_nop 0
	v_cmp_eq_u32_e32 vcc, 0, v0
	s_and_saveexec_b64 s[12:13], vcc
	s_cbranch_execz .LBB0_2366
	s_add_i32 s0, 0, 0x24800
	v_mov_b32_e32 v0, s0
	s_waitcnt vmcnt(0) expcnt(0) lgkmcnt(0)
	ds_read_b32 v1, v0
	s_add_i32 s0, 0, 0x24804
	v_mov_b32_e32 v0, s0
	ds_read_b32 v0, v0
	s_waitcnt lgkmcnt(1)
	v_cmp_ne_u32_e32 vcc, 0, v1
	s_cbranch_vccz .Lcensus_10

.LBB0_2397:
	s_cmp_lt_i32 s48, 14
	s_cselect_b64 s[0:1], -1, 0
	s_and_b64 s[0:1], s[0:1], s[4:5]
	s_andn2_b64 vcc, exec, s[0:1]
	s_cbranch_vccnz .LBB0_2762
	s_waitcnt lgkmcnt(0)
	s_mov_b32 s0, s98
	v_mbcnt_lo_u32_b32 v0, -1, 0
	v_mbcnt_hi_u32_b32 v0, -1, v0
	s_nop 1
	v_lshl_add_u32 v2, s0, 6, v0
	s_nop 0
	v_cmp_gt_i32_e32 vcc, 64, v2
	s_and_saveexec_b64 s[4:5], vcc
	s_cbranch_execz .LBB0_2417
	v_cmp_gt_i32_e32 vcc, 32, v2
	v_mov_b32_e32 v0, 0
	s_and_saveexec_b64 s[0:1], vcc
	s_cbranch_execz .LBB0_2401
	v_mov_b32_e32 v0, 0x800
	v_lshl_add_u32 v0, v2, 6, v0
	v_ashrrev_i32_e32 v1, 31, v0
	v_lshl_add_u64 v[0:1], v[0:1], 2, s[78:79]
	global_load_dword v0, v[0:1], off

.LBB0_2417:
	s_or_b64 exec, exec, s[4:5]
	s_add_i32 s3, 0, 0x24000
	v_mov_b32_e32 v0, s3
	s_waitcnt vmcnt(0) lgkmcnt(0)
	s_barrier
	ds_read_b32 v0, v0
	s_and_b32 s5, s33, 7
	s_waitcnt lgkmcnt(0)
	v_readfirstlane_b32 s4, v0
	v_mbcnt_lo_u32_b32 v0, -1, 0
	v_mbcnt_hi_u32_b32 v0, -1, v0
	s_cmp_eq_u32 s5, 0
	s_waitcnt lgkmcnt(0)
	s_mov_b32 s0, s98
	s_mov_b32 s16, s2
	s_nop 0
	v_lshl_add_u32 v8, s0, 6, v0
	s_cselect_b64 s[0:1], -1, 0
	v_readfirstlane_b32 s18, v8
	s_cmp_lg_u32 s5, 0
	s_cbranch_scc1 .LBB0_2419
	s_and_b32 s5, s2, 7
	s_ashr_i32 s12, s33, 3
	s_mul_i32 s5, s12, s5
	s_ashr_i32 s12, s2, 3
	s_add_i32 s16, s5, s12

.LBB0_2600:
	v_mov_b32_e32 v1, s3
	v_mbcnt_lo_u32_b32 v2, -1, 0
	v_mbcnt_hi_u32_b32 v2, -1, v2
	s_waitcnt lgkmcnt(0)
	s_mov_b32 s0, s98
	s_nop 1
	v_lshl_add_u32 v6, s0, 6, v2
	ds_read_b32 v0, v1
	s_ashr_i32 s0, s2, 1
	s_add_i32 s15, s29, s0
	v_readfirstlane_b32 s22, v6
	s_waitcnt lgkmcnt(0)
	v_lshlrev_b32_e32 v0, 1, v0
	v_cmp_ge_i32_e32 vcc, s15, v0
	s_cbranch_vccnz .LBB0_2687
	s_and_b32 s0, s22, 0xffffffc0
	v_mbcnt_lo_u32_b32 v0, -1, 0
	v_mbcnt_hi_u32_b32 v0, -1, v0
	s_ashr_i32 s18, s15, 1
	v_add_u32_e32 v0, s0, v0
	s_lshl_b32 s0, s18, 2
	v_ashrrev_i32_e32 v2, 31, v0
	v_lshrrev_b32_e32 v2, 26, v2
	v_add_u32_e32 v2, v0, v2
	v_lshlrev_b32_e32 v1, 4, v0
	v_ashrrev_i32_e32 v2, 6, v2
	v_bfe_i32 v0, v0, 27, 1
	v_lshrrev_b32_e32 v0, 22, v0
	v_lshlrev_b32_e32 v2, 3, v2
	s_add_i32 s0, s3, s0
	v_add_u32_e32 v0, v1, v0
	v_and_b32_e32 v4, -16, v2
	v_mov_b32_e32 v2, s0
	v_and_b32_e32 v0, 0xfffffc00, v0
	ds_read2_b32 v[2:3], v2 offset0:64 offset1:224
	v_sub_u32_e32 v0, v1, v0
	v_lshrrev_b32_e32 v1, 4, v0
	v_ashrrev_i32_e32 v5, 31, v0
	v_and_b32_e32 v1, 32, v1
	v_lshrrev_b32_e32 v5, 26, v5
	v_xad_u32 v0, v1, v0, v5
	v_ashrrev_i32_e32 v5, 6, v0
	s_waitcnt lgkmcnt(0)
	v_ashrrev_i32_e32 v1, 31, v2
	v_mov_b32_e32 v0, v2
	v_lshlrev_b32_e32 v2, 2, v2
	v_add_u32_e32 v2, s3, v2
	ds_read_b32 v9, v2 offset:4
	s_and_b32 s20, s2, 1
	s_lshl_b32 s0, s20, 7
	v_add_u32_e32 v2, s0, v3
	v_add3_u32 v4, v2, v4, v5
	v_lshlrev_b64 v[2:3], 16, v[0:1]
	v_lshl_add_u64 v[2:3], s[6:7], 0, v[2:3]
	s_waitcnt lgkmcnt(0)
	v_cmp_lt_i32_e32 vcc, v4, v9
	v_mov_b32_e32 v7, 0
	v_mov_b32_e32 v8, 0
	s_and_saveexec_b64 s[0:1], vcc
	s_cbranch_execz .LBB0_2603
	v_ashrrev_i32_e32 v5, 31, v4
	v_lshl_add_u64 v[10:11], v[4:5], 2, v[2:3]
	global_load_dword v5, v[10:11], off
	s_waitcnt vmcnt(0)
	v_lshlrev_b32_e32 v5, 9, v5
	v_and_b32_e32 v8, 0x3fffc00, v5

.LBB0_2687:
	s_sub_i32 s0, s28, s29
	s_ashr_i32 s24, s29, 1
	s_lshl_b32 s25, s0, 1
	s_cmp_ge_i32 s2, s25
	s_waitcnt lgkmcnt(0)
	s_mov_b32 s0, s98
	v_mbcnt_lo_u32_b32 v1, -1, 0
	v_mbcnt_hi_u32_b32 v1, -1, v1
	s_nop 1
	v_lshl_add_u32 v0, s0, 6, v1
	s_cselect_b64 s[0:1], -1, 0
	s_and_b64 vcc, exec, s[0:1]
	v_readfirstlane_b32 s19, v0
	s_cbranch_vccz .LBB0_2690
	s_sub_i32 s10, s2, s25
	s_lshl_b32 s4, s24, 2
	s_mov_b64 s[8:9], 0
	s_cmp_ge_i32 s10, s4
	s_mov_b64 s[4:5], 0
	s_cbranch_scc1 .LBB0_2691
	s_and_b32 s36, s10, 3
	s_ashr_i32 s38, s10, 2
	s_mov_b64 s[4:5], -1
	s_branch .LBB0_2691

.LBB0_2762:
	v_readlane_b32 s4, v249, 51
	v_readlane_b32 s5, v249, 52
	s_mov_b64 s[44:45], s[4:5]
	s_cmp_lt_i32 s44, 15
	v_readlane_b32 s6, v249, 53
	v_readlane_b32 s7, v249, 54
	s_cselect_b64 s[0:1], -1, 0
	s_cmp_gt_i32 s45, 15
	s_cselect_b64 s[6:7], -1, 0
	s_and_b64 s[0:1], s[0:1], s[6:7]
	s_andn2_b64 vcc, exec, s[0:1]
	s_cbranch_vccnz .LBB0_2822
	s_waitcnt vmcnt(0)
	s_waitcnt vmcnt(0) lgkmcnt(0)
	s_barrier
	s_waitcnt lgkmcnt(0)
	s_mov_b32 s0, s98
	v_mbcnt_lo_u32_b32 v0, -1, 0
	v_mbcnt_hi_u32_b32 v0, -1, v0
	s_nop 1
	v_lshl_add_u32 v0, s0, 6, v0
	s_nop 0
	v_cmp_eq_u32_e32 vcc, 0, v0
	s_and_saveexec_b64 s[4:5], vcc
	s_cbranch_execz .LBB0_2791
	s_add_i32 s0, 0, 0x24800
	v_mov_b32_e32 v0, s0
	s_waitcnt vmcnt(0) expcnt(0) lgkmcnt(0)
	ds_read_b32 v1, v0
	s_add_i32 s0, 0, 0x24804
	v_mov_b32_e32 v0, s0
	ds_read_b32 v0, v0
	s_waitcnt lgkmcnt(1)
	v_cmp_ne_u32_e32 vcc, 0, v1
	s_cbranch_vccz .Lcensus_11

.LBB0_2822:
	s_cmp_lt_i32 s44, 16
	s_cselect_b64 s[4:5], -1, 0
	s_and_b64 s[0:1], s[4:5], s[6:7]
	s_andn2_b64 vcc, exec, s[0:1]
	s_cbranch_vccnz .LBB0_2866
	v_mbcnt_lo_u32_b32 v1, -1, 0
	v_mbcnt_hi_u32_b32 v1, -1, v1
	s_lshl_b32 s0, s2, 3
	s_movk_i32 s35, 0x4000
	s_waitcnt lgkmcnt(0)
	s_mov_b32 s1, s98
	s_nop 1
	v_lshl_add_u32 v1, s1, 6, v1
	s_nop 0
	v_ashrrev_i32_e32 v0, 6, v1
	v_add_u32_e32 v117, s0, v0
	v_cmp_gt_i32_e32 vcc, s35, v117
	s_and_saveexec_b64 s[6:7], vcc
	s_cbranch_execz .LBB0_2865
	s_lshl_b32 s37, s33, 3
	s_cmp_eq_u64 s[76:77], 0
	v_readlane_b32 s48, v249, 2
	s_cselect_b64 s[10:11], -1, 0
	s_cmp_lg_u64 s[76:77], 0
	v_readlane_b32 s58, v249, 12
	v_readlane_b32 s59, v249, 13
	s_cselect_b64 s[12:13], -1, 0
	s_lshl_b32 s14, s33, 4
	s_mov_b64 s[18:19], s[58:59]
	v_readlane_b32 s60, v249, 14
	v_readlane_b32 s61, v249, 15
	s_add_u32 s2, s18, 0x3000
	s_mov_b64 s[20:21], s[60:61]
	s_addc_u32 s3, s19, 0
	v_lshlrev_b32_e32 v2, 3, v1
	s_add_u32 s18, s20, 0x3000
	v_and_b32_e32 v112, 0x1f8, v2
	s_addc_u32 s19, s21, 0
	v_mov_b32_e32 v115, 0
	v_lshlrev_b32_e32 v114, 2, v112
	v_or_b32_e32 v122, 4, v112
	v_or_b32_e32 v116, 0x200, v112
	v_lshl_add_u64 v[118:119], s[2:3], 0, v[114:115]
	v_lshl_add_u64 v[120:121], s[18:19], 0, v[114:115]
	v_lshlrev_b32_e32 v114, 2, v122
	v_lshl_add_u64 v[124:125], s[2:3], 0, v[114:115]
	v_lshl_add_u64 v[126:127], s[18:19], 0, v[114:115]
	v_lshlrev_b32_e32 v114, 2, v116
	v_or_b32_e32 v132, 0x204, v112
	v_mov_b32_e32 v113, v115
	v_lshl_add_u64 v[128:129], s[2:3], 0, v[114:115]
	v_lshl_add_u64 v[130:131], s[18:19], 0, v[114:115]
	v_lshlrev_b32_e32 v114, 2, v132
	v_and_b32_e32 v4, 63, v1
	v_ashrrev_i32_e32 v1, 31, v0
	s_ashr_i32 s1, s0, 31
	v_lshl_add_u64 v[134:135], s[2:3], 0, v[114:115]
	v_lshl_add_u64 v[2:3], s[78:79], 0, v[112:113]
	s_mov_b64 s[2:3], 0x12500000
	v_lshl_add_u64 v[0:1], v[0:1], 0, s[0:1]
	v_lshl_add_u64 v[140:141], v[2:3], 0, s[2:3]
	v_lshlrev_b64 v[2:3], 11, v[0:1]
	v_lshlrev_b64 v[0:1], 12, v[0:1]
	v_lshl_or_b32 v0, v4, 5, v0
	v_lshl_add_u64 v[136:137], s[18:19], 0, v[114:115]
	v_lshlrev_b32_e32 v114, 1, v112
	s_ashr_i32 s15, s14, 31
	v_lshl_add_u64 v[0:1], s[76:77], 0, v[0:1]
	s_mov_b64 s[0:1], 0x800
	s_mov_b64 s[8:9], 0
	s_mov_b64 s[16:17], 0x3000
	v_lshl_add_u64 v[138:139], s[90:91], 0, v[114:115]
	v_lshlrev_b32_e32 v142, 4, v4
	v_mov_b32_e32 v143, v115
	v_lshl_add_u64 v[144:145], s[78:79], 0, v[2:3]
	s_lshl_b64 s[18:19], s[14:15], 11
	v_lshl_add_u64 v[146:147], v[0:1], 0, s[0:1]
	s_lshl_b64 s[20:21], s[14:15], 12
	v_or_b32_e32 v148, 0x12500400, v112
	v_mov_b32_e32 v149, v115
	v_mov_b32_e32 v133, -1
	s_mov_b64 s[22:23], 0x8500000
	s_mov_b32 s15, 0x8500000
	s_mov_b64 s[24:25], 0x8500400
	s_mov_b64 s[26:27], 0x4000
	s_mov_b64 s[28:29], 0x5000
	s_mov_b64 s[30:31], 0x1000
	s_mov_b32 s34, 0x3fb504f3
	s_mov_b32 s36, 0x3d000000
	v_mov_b32_e32 v113, 0x3727c5ac
	s_mov_b32 s42, 0xf800000
	v_mov_b32_e32 v123, 0x260
	s_movk_i32 s43, 0x3fff
	v_readlane_b32 s49, v249, 3
	v_readlane_b32 s50, v249, 4
	v_readlane_b32 s51, v249, 5
	v_readlane_b32 s52, v249, 6
	v_readlane_b32 s53, v249, 7
	v_readlane_b32 s54, v249, 8
	v_readlane_b32 s55, v249, 9
	v_readlane_b32 s56, v249, 10
	v_readlane_b32 s57, v249, 11
	v_readlane_b32 s62, v249, 16
	v_readlane_b32 s63, v249, 17
	s_branch .LBB0_2826

.LBB0_2866:
	s_cmp_gt_i32 s45, 16
	s_cselect_b64 s[0:1], -1, 0
	s_and_b64 s[0:1], s[4:5], s[0:1]
	s_andn2_b64 vcc, exec, s[0:1]
	s_cbranch_vccnz .LBB0_2926
	s_waitcnt vmcnt(0)
	s_waitcnt vmcnt(0) lgkmcnt(0)
	s_barrier
	s_waitcnt lgkmcnt(0)
	s_mov_b32 s0, s98
	v_mbcnt_lo_u32_b32 v0, -1, 0
	v_mbcnt_hi_u32_b32 v0, -1, v0
	s_nop 1
	v_lshl_add_u32 v0, s0, 6, v0
	s_nop 0
	v_cmp_eq_u32_e32 vcc, 0, v0
	s_and_saveexec_b64 s[2:3], vcc
	s_cbranch_execz .LBB0_2895
	s_add_i32 s0, 0, 0x24800
	v_mov_b32_e32 v0, s0
	s_waitcnt vmcnt(0) expcnt(0) lgkmcnt(0)
	ds_read_b32 v1, v0
	s_add_i32 s0, 0, 0x24804
	v_mov_b32_e32 v0, s0
	ds_read_b32 v0, v0
	s_waitcnt lgkmcnt(1)
	v_cmp_ne_u32_e32 vcc, 0, v1
	s_cbranch_vccz .Lcensus_12

.LBB0_2895:
	s_or_b64 exec, exec, s[2:3]
	s_waitcnt lgkmcnt(0)
	s_mov_b32 s0, s98
	v_mbcnt_lo_u32_b32 v0, -1, 0
	v_mbcnt_hi_u32_b32 v0, -1, v0
	s_nop 1
	v_lshl_add_u32 v0, s0, 6, v0
	s_nop 0
	v_cmp_eq_u32_e32 vcc, 0, v0
	s_and_saveexec_b64 s[0:1], vcc
	s_cbranch_execz .LBB0_2925
	s_add_i32 s2, 0, 0x24808
	v_mov_b32_e32 v0, s2
	s_add_i32 s2, 0, 0x2480c
	v_mov_b32_e32 v1, s2
	ds_read_b32 v0, v0
	ds_read_b32 v1, v1
	s_waitcnt lgkmcnt(0)
	v_cmp_eq_u32_e32 vcc, 0, v1
	s_cbranch_vccnz .LBB0_2906
	v_mov_b32_e32 v1, 0x3000
	s_add_i32 s2, 0, 0x24804
	v_mov_b32_e32 v3, s2
	ds_read_b32 v3, v3
	global_load_dword v1, v1, s[94:95] offset:1024 sc1
	s_waitcnt lgkmcnt(0)
	v_mul_lo_u32 v0, v0, v3
	s_add_u32 s2, s94, 0x3400
	s_addc_u32 s3, s95, 0
	s_waitcnt vmcnt(0)
	v_cmp_ge_u32_e32 vcc, v1, v0
	s_cbranch_vccnz .LBB0_2911
	s_mov_b32 s10, 1
	v_mov_b32_e32 v1, 0
	s_branch .LBB0_2900

	.amdhsa_kernel _Z4mega5MArgs
		.amdhsa_group_segment_fixed_size 0
		.amdhsa_private_segment_fixed_size 0
		.amdhsa_kernarg_size 496
		.amdhsa_user_sgpr_count 2
		.amdhsa_user_sgpr_dispatch_ptr 0
		.amdhsa_user_sgpr_queue_ptr 0
		.amdhsa_user_sgpr_kernarg_segment_ptr 1
		.amdhsa_user_sgpr_dispatch_id 0
		.amdhsa_user_sgpr_kernarg_preload_length 0
		.amdhsa_user_sgpr_kernarg_preload_offset 0
		.amdhsa_user_sgpr_private_segment_size 0
		.amdhsa_uses_dynamic_stack 0
		.amdhsa_enable_private_segment 0
		.amdhsa_system_sgpr_workgroup_id_x 1
		.amdhsa_system_sgpr_workgroup_id_y 0
		.amdhsa_system_sgpr_workgroup_id_z 0
		.amdhsa_system_sgpr_workgroup_info 0
		.amdhsa_system_vgpr_workitem_id 0
		.amdhsa_next_free_vgpr 250
		.amdhsa_next_free_sgpr 100
		.amdhsa_accum_offset 252
		.amdhsa_reserve_vcc 1
		.amdhsa_float_round_mode_32 0
		.amdhsa_float_round_mode_16_64 0
		.amdhsa_float_denorm_mode_32 3
		.amdhsa_float_denorm_mode_16_64 3
		.amdhsa_dx10_clamp 1
		.amdhsa_ieee_mode 1
		.amdhsa_fp16_overflow 0
		.amdhsa_tg_split 0
		.amdhsa_exception_fp_ieee_invalid_op 0
		.amdhsa_exception_fp_denorm_src 0
		.amdhsa_exception_fp_ieee_div_zero 0
		.amdhsa_exception_fp_ieee_overflow 0
		.amdhsa_exception_fp_ieee_underflow 0
		.amdhsa_exception_fp_ieee_inexact 0
		.amdhsa_exception_int_div_zero 0
	.end_amdhsa_kernel

amdhsa.kernels:
  - .agpr_count:     0
    .args:
      - .offset:         0
        .size:           240
        .value_kind:     by_value
      - .offset:         240
        .size:           4
        .value_kind:     hidden_block_count_x
      - .offset:         244
        .size:           4
        .value_kind:     hidden_block_count_y
      - .offset:         248
        .size:           4
        .value_kind:     hidden_block_count_z
      - .offset:         252
        .size:           2
        .value_kind:     hidden_group_size_x
      - .offset:         254
        .size:           2
        .value_kind:     hidden_group_size_y
      - .offset:         256
        .size:           2
        .value_kind:     hidden_group_size_z
      - .offset:         258
        .size:           2
        .value_kind:     hidden_remainder_x
      - .offset:         260
        .size:           2
        .value_kind:     hidden_remainder_y
      - .offset:         262
        .size:           2
        .value_kind:     hidden_remainder_z
      - .offset:         280
        .size:           8
        .value_kind:     hidden_global_offset_x
      - .offset:         288
        .size:           8
        .value_kind:     hidden_global_offset_y
      - .offset:         296
        .size:           8
        .value_kind:     hidden_global_offset_z
      - .offset:         304
        .size:           2
        .value_kind:     hidden_grid_dims
      - .offset:         360
        .size:           4
        .value_kind:     hidden_dynamic_lds_size
    .group_segment_fixed_size: 0
    .kernarg_segment_align: 8
    .kernarg_segment_size: 496
    .language:       OpenCL C
    .language_version:
      - 2
      - 0
    .max_flat_workgroup_size: 512
    .name:           _Z4mega5MArgs
    .private_segment_fixed_size: 0
    .sgpr_count:     106
    .sgpr_spill_count: 65
    .symbol:         _Z4mega5MArgs.kd
    .uniform_work_group_size: 1
    .uses_dynamic_stack: false
    .vgpr_count:     250
    .vgpr_spill_count: 0
    .wavefront_size: 64
